# P4 depthwise conv rewritten by hand (36 consecutive rows per wave, sliding window, all row loads in flight, pk_fma); MOE1 bias via LDS-DMA; MoE tile table in LDS; hand-written weight conversion
# speedup vs baseline: 1.0053x; 1.0053x over previous
.LBB0_1144:
	s_cmp_lt_i32 s92, 5
	s_cselect_b64 s[0:1], -1, 0
	s_cmp_gt_i32 s93, 4
	s_cselect_b64 s[2:3], -1, 0
	s_and_b64 s[0:1], s[0:1], s[2:3]
	v_cndmask_b32_e64 v0, 0, 1, s[0:1]
	v_cmp_ne_u32_e64 s[4:5], 1, v0
	s_andn2_b64 vcc, exec, s[0:1]
	v_mbcnt_lo_u32_b32 v0, -1, 0
	v_mbcnt_hi_u32_b32 v0, -1, v0
	s_cbranch_vccnz .LBB0_1155
	s_load_dword s0, s[90:91], 0x100
	s_waitcnt lgkmcnt(0)
	s_cmp_lg_u32 s0, 0x100
	s_cbranch_scc1 .Lp4_orig
	v_mbcnt_lo_u32_b32 v240, -1, 0
	v_mbcnt_hi_u32_b32 v240, -1, v240
	s_load_dwordx4 s[8:11], s[90:91], 0x48
	s_lshl_b32 s0, s94, 3
	s_add_i32 s0, s0, s97
	s_and_b32 s1, s0, 1
	s_lshr_b32 s0, s0, 1
	s_mul_i32 s6, s0, 36
	s_lshl_b32 s2, s1, 10
	v_lshlrev_b32_e32 v241, 4, v240
	v_add_u32_e32 v241, s2, v241
	s_lshl_b32 s2, s1, 11
	v_lshlrev_b32_e32 v242, 5, v240
	v_add_u32_e32 v242, s2, v242
	s_add_u32 s14, s26, 0x49800000
	s_addc_u32 s15, s27, 0
	s_waitcnt lgkmcnt(0)
	global_load_dwordx4 v[188:191], v242, s[8:9]
	global_load_dwordx4 v[192:195], v242, s[8:9] offset:16
	s_add_u32 s8, s8, 0x1000
	s_addc_u32 s9, s9, 0
	global_load_dwordx4 v[196:199], v242, s[8:9]
	global_load_dwordx4 v[200:203], v242, s[8:9] offset:16
	s_add_u32 s8, s8, 0x1000
	s_addc_u32 s9, s9, 0
	global_load_dwordx4 v[204:207], v242, s[8:9]
	global_load_dwordx4 v[208:211], v242, s[8:9] offset:16
	s_add_u32 s8, s8, 0x1000
	s_addc_u32 s9, s9, 0
	global_load_dwordx4 v[212:215], v242, s[8:9]
	global_load_dwordx4 v[216:219], v242, s[8:9] offset:16
	global_load_dwordx4 v[220:223], v242, s[10:11]
	global_load_dwordx4 v[224:227], v242, s[10:11] offset:16
	s_add_i32 s12, s6, -1
	s_max_i32 s12, s12, 0
	s_min_i32 s12, s12, 0x8fff
	s_lshl_b32 s12, s12, 11
	s_add_u32 s2, s14, s12
	s_addc_u32 s3, s15, 0
	global_load_dwordx4 v[0:3], v241, s[2:3]
	s_add_i32 s12, s6, 0
	s_max_i32 s12, s12, 0
	s_min_i32 s12, s12, 0x8fff
	s_lshl_b32 s12, s12, 11
	s_add_u32 s2, s14, s12
	s_addc_u32 s3, s15, 0
	global_load_dwordx4 v[4:7], v241, s[2:3]
	s_add_i32 s12, s6, 1
	s_max_i32 s12, s12, 0
	s_min_i32 s12, s12, 0x8fff
	s_lshl_b32 s12, s12, 11
	s_add_u32 s2, s14, s12
	s_addc_u32 s3, s15, 0
	global_load_dwordx4 v[8:11], v241, s[2:3]
	s_add_i32 s12, s6, 2
	s_max_i32 s12, s12, 0
	s_min_i32 s12, s12, 0x8fff
	s_lshl_b32 s12, s12, 11
	s_add_u32 s2, s14, s12
	s_addc_u32 s3, s15, 0
	global_load_dwordx4 v[12:15], v241, s[2:3]
	s_add_i32 s12, s6, 3
	s_max_i32 s12, s12, 0
	s_min_i32 s12, s12, 0x8fff
	s_lshl_b32 s12, s12, 11
	s_add_u32 s2, s14, s12
	s_addc_u32 s3, s15, 0
	global_load_dwordx4 v[16:19], v241, s[2:3]
	s_add_i32 s12, s6, 4
	s_max_i32 s12, s12, 0
	s_min_i32 s12, s12, 0x8fff
	s_lshl_b32 s12, s12, 11
	s_add_u32 s2, s14, s12
	s_addc_u32 s3, s15, 0
	global_load_dwordx4 v[20:23], v241, s[2:3]
	s_add_i32 s12, s6, 5
	s_max_i32 s12, s12, 0
	s_min_i32 s12, s12, 0x8fff
	s_lshl_b32 s12, s12, 11
	s_add_u32 s2, s14, s12
	s_addc_u32 s3, s15, 0
	global_load_dwordx4 v[24:27], v241, s[2:3]
	s_add_i32 s12, s6, 6
	s_max_i32 s12, s12, 0
	s_min_i32 s12, s12, 0x8fff
	s_lshl_b32 s12, s12, 11
	s_add_u32 s2, s14, s12
	s_addc_u32 s3, s15, 0
	global_load_dwordx4 v[28:31], v241, s[2:3]
	s_add_i32 s12, s6, 7
	s_max_i32 s12, s12, 0
	s_min_i32 s12, s12, 0x8fff
	s_lshl_b32 s12, s12, 11
	s_add_u32 s2, s14, s12
	s_addc_u32 s3, s15, 0
	global_load_dwordx4 v[32:35], v241, s[2:3]
	s_add_i32 s12, s6, 8
	s_max_i32 s12, s12, 0
	s_min_i32 s12, s12, 0x8fff
	s_lshl_b32 s12, s12, 11
	s_add_u32 s2, s14, s12
	s_addc_u32 s3, s15, 0
	global_load_dwordx4 v[36:39], v241, s[2:3]
	s_add_i32 s12, s6, 9
	s_max_i32 s12, s12, 0
	s_min_i32 s12, s12, 0x8fff
	s_lshl_b32 s12, s12, 11
	s_add_u32 s2, s14, s12
	s_addc_u32 s3, s15, 0
	global_load_dwordx4 v[40:43], v241, s[2:3]
	s_add_i32 s12, s6, 10
	s_max_i32 s12, s12, 0
	s_min_i32 s12, s12, 0x8fff
	s_lshl_b32 s12, s12, 11
	s_add_u32 s2, s14, s12
	s_addc_u32 s3, s15, 0
	global_load_dwordx4 v[44:47], v241, s[2:3]
	s_add_i32 s12, s6, 11
	s_max_i32 s12, s12, 0
	s_min_i32 s12, s12, 0x8fff
	s_lshl_b32 s12, s12, 11
	s_add_u32 s2, s14, s12
	s_addc_u32 s3, s15, 0
	global_load_dwordx4 v[48:51], v241, s[2:3]
	s_add_i32 s12, s6, 12
	s_max_i32 s12, s12, 0
	s_min_i32 s12, s12, 0x8fff
	s_lshl_b32 s12, s12, 11
	s_add_u32 s2, s14, s12
	s_addc_u32 s3, s15, 0
	global_load_dwordx4 v[52:55], v241, s[2:3]
	s_add_i32 s12, s6, 13
	s_max_i32 s12, s12, 0
	s_min_i32 s12, s12, 0x8fff
	s_lshl_b32 s12, s12, 11
	s_add_u32 s2, s14, s12
	s_addc_u32 s3, s15, 0
	global_load_dwordx4 v[56:59], v241, s[2:3]
	s_add_i32 s12, s6, 14
	s_max_i32 s12, s12, 0
	s_min_i32 s12, s12, 0x8fff
	s_lshl_b32 s12, s12, 11
	s_add_u32 s2, s14, s12
	s_addc_u32 s3, s15, 0
	global_load_dwordx4 v[60:63], v241, s[2:3]
	s_add_i32 s12, s6, 15
	s_max_i32 s12, s12, 0
	s_min_i32 s12, s12, 0x8fff
	s_lshl_b32 s12, s12, 11
	s_add_u32 s2, s14, s12
	s_addc_u32 s3, s15, 0
	global_load_dwordx4 v[64:67], v241, s[2:3]
	s_add_i32 s12, s6, 16
	s_max_i32 s12, s12, 0
	s_min_i32 s12, s12, 0x8fff
	s_lshl_b32 s12, s12, 11
	s_add_u32 s2, s14, s12
	s_addc_u32 s3, s15, 0
	global_load_dwordx4 v[68:71], v241, s[2:3]
	s_add_i32 s12, s6, 17
	s_max_i32 s12, s12, 0
	s_min_i32 s12, s12, 0x8fff
	s_lshl_b32 s12, s12, 11
	s_add_u32 s2, s14, s12
	s_addc_u32 s3, s15, 0
	global_load_dwordx4 v[72:75], v241, s[2:3]
	s_add_i32 s12, s6, 18
	s_max_i32 s12, s12, 0
	s_min_i32 s12, s12, 0x8fff
	s_lshl_b32 s12, s12, 11
	s_add_u32 s2, s14, s12
	s_addc_u32 s3, s15, 0
	global_load_dwordx4 v[76:79], v241, s[2:3]
	s_add_i32 s12, s6, 19
	s_max_i32 s12, s12, 0
	s_min_i32 s12, s12, 0x8fff
	s_lshl_b32 s12, s12, 11
	s_add_u32 s2, s14, s12
	s_addc_u32 s3, s15, 0
	global_load_dwordx4 v[80:83], v241, s[2:3]
	s_add_i32 s12, s6, 20
	s_max_i32 s12, s12, 0
	s_min_i32 s12, s12, 0x8fff
	s_lshl_b32 s12, s12, 11
	s_add_u32 s2, s14, s12
	s_addc_u32 s3, s15, 0
	global_load_dwordx4 v[84:87], v241, s[2:3]
	s_add_i32 s12, s6, 21
	s_max_i32 s12, s12, 0
	s_min_i32 s12, s12, 0x8fff
	s_lshl_b32 s12, s12, 11
	s_add_u32 s2, s14, s12
	s_addc_u32 s3, s15, 0
	global_load_dwordx4 v[88:91], v241, s[2:3]
	s_add_i32 s12, s6, 22
	s_max_i32 s12, s12, 0
	s_min_i32 s12, s12, 0x8fff
	s_lshl_b32 s12, s12, 11
	s_add_u32 s2, s14, s12
	s_addc_u32 s3, s15, 0
	global_load_dwordx4 v[92:95], v241, s[2:3]
	s_add_i32 s12, s6, 23
	s_max_i32 s12, s12, 0
	s_min_i32 s12, s12, 0x8fff
	s_lshl_b32 s12, s12, 11
	s_add_u32 s2, s14, s12
	s_addc_u32 s3, s15, 0
	global_load_dwordx4 v[96:99], v241, s[2:3]
	s_add_i32 s12, s6, 24
	s_max_i32 s12, s12, 0
	s_min_i32 s12, s12, 0x8fff
	s_lshl_b32 s12, s12, 11
	s_add_u32 s2, s14, s12
	s_addc_u32 s3, s15, 0
	global_load_dwordx4 v[100:103], v241, s[2:3]
	s_add_i32 s12, s6, 25
	s_max_i32 s12, s12, 0
	s_min_i32 s12, s12, 0x8fff
	s_lshl_b32 s12, s12, 11
	s_add_u32 s2, s14, s12
	s_addc_u32 s3, s15, 0
	global_load_dwordx4 v[104:107], v241, s[2:3]
	s_add_i32 s12, s6, 26
	s_max_i32 s12, s12, 0
	s_min_i32 s12, s12, 0x8fff
	s_lshl_b32 s12, s12, 11
	s_add_u32 s2, s14, s12
	s_addc_u32 s3, s15, 0
	global_load_dwordx4 v[108:111], v241, s[2:3]
	s_add_i32 s12, s6, 27
	s_max_i32 s12, s12, 0
	s_min_i32 s12, s12, 0x8fff
	s_lshl_b32 s12, s12, 11
	s_add_u32 s2, s14, s12
	s_addc_u32 s3, s15, 0
	global_load_dwordx4 v[112:115], v241, s[2:3]
	s_add_i32 s12, s6, 28
	s_max_i32 s12, s12, 0
	s_min_i32 s12, s12, 0x8fff
	s_lshl_b32 s12, s12, 11
	s_add_u32 s2, s14, s12
	s_addc_u32 s3, s15, 0
	global_load_dwordx4 v[116:119], v241, s[2:3]
	s_add_i32 s12, s6, 29
	s_max_i32 s12, s12, 0
	s_min_i32 s12, s12, 0x8fff
	s_lshl_b32 s12, s12, 11
	s_add_u32 s2, s14, s12
	s_addc_u32 s3, s15, 0
	global_load_dwordx4 v[120:123], v241, s[2:3]
	s_add_i32 s12, s6, 30
	s_max_i32 s12, s12, 0
	s_min_i32 s12, s12, 0x8fff
	s_lshl_b32 s12, s12, 11
	s_add_u32 s2, s14, s12
	s_addc_u32 s3, s15, 0
	global_load_dwordx4 v[124:127], v241, s[2:3]
	s_add_i32 s12, s6, 31
	s_max_i32 s12, s12, 0
	s_min_i32 s12, s12, 0x8fff
	s_lshl_b32 s12, s12, 11
	s_add_u32 s2, s14, s12
	s_addc_u32 s3, s15, 0
	global_load_dwordx4 v[128:131], v241, s[2:3]
	s_add_i32 s12, s6, 32
	s_max_i32 s12, s12, 0
	s_min_i32 s12, s12, 0x8fff
	s_lshl_b32 s12, s12, 11
	s_add_u32 s2, s14, s12
	s_addc_u32 s3, s15, 0
	global_load_dwordx4 v[132:135], v241, s[2:3]
	s_add_i32 s12, s6, 33
	s_max_i32 s12, s12, 0
	s_min_i32 s12, s12, 0x8fff
	s_lshl_b32 s12, s12, 11
	s_add_u32 s2, s14, s12
	s_addc_u32 s3, s15, 0
	global_load_dwordx4 v[136:139], v241, s[2:3]
	s_add_i32 s12, s6, 34
	s_max_i32 s12, s12, 0
	s_min_i32 s12, s12, 0x8fff
	s_lshl_b32 s12, s12, 11
	s_add_u32 s2, s14, s12
	s_addc_u32 s3, s15, 0
	global_load_dwordx4 v[140:143], v241, s[2:3]
	s_add_i32 s12, s6, 35
	s_max_i32 s12, s12, 0
	s_min_i32 s12, s12, 0x8fff
	s_lshl_b32 s12, s12, 11
	s_add_u32 s2, s14, s12
	s_addc_u32 s3, s15, 0
	global_load_dwordx4 v[144:147], v241, s[2:3]
	s_add_i32 s12, s6, 36
	s_max_i32 s12, s12, 0
	s_min_i32 s12, s12, 0x8fff
	s_lshl_b32 s12, s12, 11
	s_add_u32 s2, s14, s12
	s_addc_u32 s3, s15, 0
	global_load_dwordx4 v[148:151], v241, s[2:3]
	s_add_i32 s12, s6, 37
	s_max_i32 s12, s12, 0
	s_min_i32 s12, s12, 0x8fff
	s_lshl_b32 s12, s12, 11
	s_add_u32 s2, s14, s12
	s_addc_u32 s3, s15, 0
	global_load_dwordx4 v[152:155], v241, s[2:3]
	s_add_u32 s8, s26, 0x70800000
	s_addc_u32 s9, s27, 0
	s_waitcnt vmcnt(36)
	v_lshlrev_b32_e32 v156, 16, v0
	v_and_b32_e32 v157, 0xffff0000, v0
	v_lshlrev_b32_e32 v158, 16, v1
	v_and_b32_e32 v159, 0xffff0000, v1
	v_lshlrev_b32_e32 v160, 16, v2
	v_and_b32_e32 v161, 0xffff0000, v2
	v_lshlrev_b32_e32 v162, 16, v3
	v_and_b32_e32 v163, 0xffff0000, v3
	v_lshlrev_b32_e32 v164, 16, v4
	v_and_b32_e32 v165, 0xffff0000, v4
	v_lshlrev_b32_e32 v166, 16, v5
	v_and_b32_e32 v167, 0xffff0000, v5
	v_lshlrev_b32_e32 v168, 16, v6
	v_and_b32_e32 v169, 0xffff0000, v6
	v_lshlrev_b32_e32 v170, 16, v7
	v_and_b32_e32 v171, 0xffff0000, v7
	v_lshlrev_b32_e32 v172, 16, v8
	v_and_b32_e32 v173, 0xffff0000, v8
	v_lshlrev_b32_e32 v174, 16, v9
	v_and_b32_e32 v175, 0xffff0000, v9
	v_lshlrev_b32_e32 v176, 16, v10
	v_and_b32_e32 v177, 0xffff0000, v10
	v_lshlrev_b32_e32 v178, 16, v11
	v_and_b32_e32 v179, 0xffff0000, v11
	s_waitcnt vmcnt(35)
	v_lshlrev_b32_e32 v180, 16, v12
	v_and_b32_e32 v181, 0xffff0000, v12
	v_lshlrev_b32_e32 v182, 16, v13
	v_and_b32_e32 v183, 0xffff0000, v13
	v_lshlrev_b32_e32 v184, 16, v14
	v_and_b32_e32 v185, 0xffff0000, v14
	v_lshlrev_b32_e32 v186, 16, v15
	v_and_b32_e32 v187, 0xffff0000, v15
	s_add_i32 s12, s6, 0
	s_movk_i32 s13, 0xff
	s_cmp_lt_u32 s12, 0x8000
	s_cselect_b32 s13, 0x7ff, s13
	s_and_b32 s16, s12, s13
	s_cmp_lg_u32 s16, 0
	s_cbranch_scc0 .Lp4_nm1_0
	v_pk_fma_f32 v[228:229], v[156:157], v[188:189], v[220:221]
	v_pk_fma_f32 v[230:231], v[158:159], v[190:191], v[222:223]
	v_pk_fma_f32 v[232:233], v[160:161], v[192:193], v[224:225]
	v_pk_fma_f32 v[234:235], v[162:163], v[194:195], v[226:227]
	v_pk_fma_f32 v[228:229], v[164:165], v[196:197], v[228:229]
	v_pk_fma_f32 v[230:231], v[166:167], v[198:199], v[230:231]
	v_pk_fma_f32 v[232:233], v[168:169], v[200:201], v[232:233]
	v_pk_fma_f32 v[234:235], v[170:171], v[202:203], v[234:235]
	s_branch .Lp4_j0_0
.Lp4_nm1_0:
	v_pk_fma_f32 v[228:229], v[164:165], v[196:197], v[220:221]
	v_pk_fma_f32 v[230:231], v[166:167], v[198:199], v[222:223]
	v_pk_fma_f32 v[232:233], v[168:169], v[200:201], v[224:225]
	v_pk_fma_f32 v[234:235], v[170:171], v[202:203], v[226:227]
.Lp4_j0_0:
	s_cmp_lg_u32 s16, s13
	s_cbranch_scc0 .Lp4_j1_0
	v_pk_fma_f32 v[228:229], v[172:173], v[204:205], v[228:229]
	v_pk_fma_f32 v[230:231], v[174:175], v[206:207], v[230:231]
	v_pk_fma_f32 v[232:233], v[176:177], v[208:209], v[232:233]
	v_pk_fma_f32 v[234:235], v[178:179], v[210:211], v[234:235]
.Lp4_j1_0:
	s_add_i32 s17, s16, 2
	s_cmp_le_u32 s17, s13
	s_cbranch_scc0 .Lp4_j2_0
	v_pk_fma_f32 v[228:229], v[180:181], v[212:213], v[228:229]
	v_pk_fma_f32 v[230:231], v[182:183], v[214:215], v[230:231]
	v_pk_fma_f32 v[232:233], v[184:185], v[216:217], v[232:233]
	v_pk_fma_f32 v[234:235], v[186:187], v[218:219], v[234:235]
.Lp4_j2_0:
	v_cvt_pk_bf16_f32 v236, v228, v229
	v_cvt_pk_bf16_f32 v237, v230, v231
	v_cvt_pk_bf16_f32 v238, v232, v233
	v_cvt_pk_bf16_f32 v239, v234, v235
	s_lshl_b32 s17, s12, 11
	s_add_u32 s2, s8, s17
	s_addc_u32 s3, s9, 0
	global_store_dwordx4 v241, v[236:239], s[2:3]
	s_waitcnt vmcnt(35)
	v_lshlrev_b32_e32 v156, 16, v16
	v_and_b32_e32 v157, 0xffff0000, v16
	v_lshlrev_b32_e32 v158, 16, v17
	v_and_b32_e32 v159, 0xffff0000, v17
	v_lshlrev_b32_e32 v160, 16, v18
	v_and_b32_e32 v161, 0xffff0000, v18
	v_lshlrev_b32_e32 v162, 16, v19
	v_and_b32_e32 v163, 0xffff0000, v19
	s_add_i32 s12, s6, 1
	s_movk_i32 s13, 0xff
	s_cmp_lt_u32 s12, 0x8000
	s_cselect_b32 s13, 0x7ff, s13
	s_and_b32 s16, s12, s13
	s_cmp_lg_u32 s16, 0
	s_cbranch_scc0 .Lp4_nm1_1
	v_pk_fma_f32 v[228:229], v[164:165], v[188:189], v[220:221]
	v_pk_fma_f32 v[230:231], v[166:167], v[190:191], v[222:223]
	v_pk_fma_f32 v[232:233], v[168:169], v[192:193], v[224:225]
	v_pk_fma_f32 v[234:235], v[170:171], v[194:195], v[226:227]
	v_pk_fma_f32 v[228:229], v[172:173], v[196:197], v[228:229]
	v_pk_fma_f32 v[230:231], v[174:175], v[198:199], v[230:231]
	v_pk_fma_f32 v[232:233], v[176:177], v[200:201], v[232:233]
	v_pk_fma_f32 v[234:235], v[178:179], v[202:203], v[234:235]
	s_branch .Lp4_j0_1
.Lp4_nm1_1:
	v_pk_fma_f32 v[228:229], v[172:173], v[196:197], v[220:221]
	v_pk_fma_f32 v[230:231], v[174:175], v[198:199], v[222:223]
	v_pk_fma_f32 v[232:233], v[176:177], v[200:201], v[224:225]
	v_pk_fma_f32 v[234:235], v[178:179], v[202:203], v[226:227]
.Lp4_j0_1:
	s_cmp_lg_u32 s16, s13
	s_cbranch_scc0 .Lp4_j1_1
	v_pk_fma_f32 v[228:229], v[180:181], v[204:205], v[228:229]
	v_pk_fma_f32 v[230:231], v[182:183], v[206:207], v[230:231]
	v_pk_fma_f32 v[232:233], v[184:185], v[208:209], v[232:233]
	v_pk_fma_f32 v[234:235], v[186:187], v[210:211], v[234:235]
.Lp4_j1_1:
	s_add_i32 s17, s16, 2
	s_cmp_le_u32 s17, s13
	s_cbranch_scc0 .Lp4_j2_1
	v_pk_fma_f32 v[228:229], v[156:157], v[212:213], v[228:229]
	v_pk_fma_f32 v[230:231], v[158:159], v[214:215], v[230:231]
	v_pk_fma_f32 v[232:233], v[160:161], v[216:217], v[232:233]
	v_pk_fma_f32 v[234:235], v[162:163], v[218:219], v[234:235]
.Lp4_j2_1:
	v_cvt_pk_bf16_f32 v236, v228, v229
	v_cvt_pk_bf16_f32 v237, v230, v231
	v_cvt_pk_bf16_f32 v238, v232, v233
	v_cvt_pk_bf16_f32 v239, v234, v235
	s_lshl_b32 s17, s12, 11
	s_add_u32 s2, s8, s17
	s_addc_u32 s3, s9, 0
	global_store_dwordx4 v241, v[236:239], s[2:3]
	s_waitcnt vmcnt(35)
	v_lshlrev_b32_e32 v164, 16, v20
	v_and_b32_e32 v165, 0xffff0000, v20
	v_lshlrev_b32_e32 v166, 16, v21
	v_and_b32_e32 v167, 0xffff0000, v21
	v_lshlrev_b32_e32 v168, 16, v22
	v_and_b32_e32 v169, 0xffff0000, v22
	v_lshlrev_b32_e32 v170, 16, v23
	v_and_b32_e32 v171, 0xffff0000, v23
	s_add_i32 s12, s6, 2
	s_movk_i32 s13, 0xff
	s_cmp_lt_u32 s12, 0x8000
	s_cselect_b32 s13, 0x7ff, s13
	s_and_b32 s16, s12, s13
	s_cmp_lg_u32 s16, 0
	s_cbranch_scc0 .Lp4_nm1_2
	v_pk_fma_f32 v[228:229], v[172:173], v[188:189], v[220:221]
	v_pk_fma_f32 v[230:231], v[174:175], v[190:191], v[222:223]
	v_pk_fma_f32 v[232:233], v[176:177], v[192:193], v[224:225]
	v_pk_fma_f32 v[234:235], v[178:179], v[194:195], v[226:227]
	v_pk_fma_f32 v[228:229], v[180:181], v[196:197], v[228:229]
	v_pk_fma_f32 v[230:231], v[182:183], v[198:199], v[230:231]
	v_pk_fma_f32 v[232:233], v[184:185], v[200:201], v[232:233]
	v_pk_fma_f32 v[234:235], v[186:187], v[202:203], v[234:235]
	s_branch .Lp4_j0_2
.Lp4_nm1_2:
	v_pk_fma_f32 v[228:229], v[180:181], v[196:197], v[220:221]
	v_pk_fma_f32 v[230:231], v[182:183], v[198:199], v[222:223]
	v_pk_fma_f32 v[232:233], v[184:185], v[200:201], v[224:225]
	v_pk_fma_f32 v[234:235], v[186:187], v[202:203], v[226:227]
.Lp4_j0_2:
	s_cmp_lg_u32 s16, s13
	s_cbranch_scc0 .Lp4_j1_2
	v_pk_fma_f32 v[228:229], v[156:157], v[204:205], v[228:229]
	v_pk_fma_f32 v[230:231], v[158:159], v[206:207], v[230:231]
	v_pk_fma_f32 v[232:233], v[160:161], v[208:209], v[232:233]
	v_pk_fma_f32 v[234:235], v[162:163], v[210:211], v[234:235]
.Lp4_j1_2:
	s_add_i32 s17, s16, 2
	s_cmp_le_u32 s17, s13
	s_cbranch_scc0 .Lp4_j2_2
	v_pk_fma_f32 v[228:229], v[164:165], v[212:213], v[228:229]
	v_pk_fma_f32 v[230:231], v[166:167], v[214:215], v[230:231]
	v_pk_fma_f32 v[232:233], v[168:169], v[216:217], v[232:233]
	v_pk_fma_f32 v[234:235], v[170:171], v[218:219], v[234:235]
.Lp4_j2_2:
	v_cvt_pk_bf16_f32 v236, v228, v229
	v_cvt_pk_bf16_f32 v237, v230, v231
	v_cvt_pk_bf16_f32 v238, v232, v233
	v_cvt_pk_bf16_f32 v239, v234, v235
	s_lshl_b32 s17, s12, 11
	s_add_u32 s2, s8, s17
	s_addc_u32 s3, s9, 0
	global_store_dwordx4 v241, v[236:239], s[2:3]
	s_waitcnt vmcnt(35)
	v_lshlrev_b32_e32 v172, 16, v24
	v_and_b32_e32 v173, 0xffff0000, v24
	v_lshlrev_b32_e32 v174, 16, v25
	v_and_b32_e32 v175, 0xffff0000, v25
	v_lshlrev_b32_e32 v176, 16, v26
	v_and_b32_e32 v177, 0xffff0000, v26
	v_lshlrev_b32_e32 v178, 16, v27
	v_and_b32_e32 v179, 0xffff0000, v27
	s_add_i32 s12, s6, 3
	s_movk_i32 s13, 0xff
	s_cmp_lt_u32 s12, 0x8000
	s_cselect_b32 s13, 0x7ff, s13
	s_and_b32 s16, s12, s13
	s_cmp_lg_u32 s16, 0
	s_cbranch_scc0 .Lp4_nm1_3
	v_pk_fma_f32 v[228:229], v[180:181], v[188:189], v[220:221]
	v_pk_fma_f32 v[230:231], v[182:183], v[190:191], v[222:223]
	v_pk_fma_f32 v[232:233], v[184:185], v[192:193], v[224:225]
	v_pk_fma_f32 v[234:235], v[186:187], v[194:195], v[226:227]
	v_pk_fma_f32 v[228:229], v[156:157], v[196:197], v[228:229]
	v_pk_fma_f32 v[230:231], v[158:159], v[198:199], v[230:231]
	v_pk_fma_f32 v[232:233], v[160:161], v[200:201], v[232:233]
	v_pk_fma_f32 v[234:235], v[162:163], v[202:203], v[234:235]
	s_branch .Lp4_j0_3
.Lp4_nm1_3:
	v_pk_fma_f32 v[228:229], v[156:157], v[196:197], v[220:221]
	v_pk_fma_f32 v[230:231], v[158:159], v[198:199], v[222:223]
	v_pk_fma_f32 v[232:233], v[160:161], v[200:201], v[224:225]
	v_pk_fma_f32 v[234:235], v[162:163], v[202:203], v[226:227]
.Lp4_j0_3:
	s_cmp_lg_u32 s16, s13
	s_cbranch_scc0 .Lp4_j1_3
	v_pk_fma_f32 v[228:229], v[164:165], v[204:205], v[228:229]
	v_pk_fma_f32 v[230:231], v[166:167], v[206:207], v[230:231]
	v_pk_fma_f32 v[232:233], v[168:169], v[208:209], v[232:233]
	v_pk_fma_f32 v[234:235], v[170:171], v[210:211], v[234:235]
.Lp4_j1_3:
	s_add_i32 s17, s16, 2
	s_cmp_le_u32 s17, s13
	s_cbranch_scc0 .Lp4_j2_3
	v_pk_fma_f32 v[228:229], v[172:173], v[212:213], v[228:229]
	v_pk_fma_f32 v[230:231], v[174:175], v[214:215], v[230:231]
	v_pk_fma_f32 v[232:233], v[176:177], v[216:217], v[232:233]
	v_pk_fma_f32 v[234:235], v[178:179], v[218:219], v[234:235]
.Lp4_j2_3:
	v_cvt_pk_bf16_f32 v236, v228, v229
	v_cvt_pk_bf16_f32 v237, v230, v231
	v_cvt_pk_bf16_f32 v238, v232, v233
	v_cvt_pk_bf16_f32 v239, v234, v235
	s_lshl_b32 s17, s12, 11
	s_add_u32 s2, s8, s17
	s_addc_u32 s3, s9, 0
	global_store_dwordx4 v241, v[236:239], s[2:3]
	s_waitcnt vmcnt(35)
	v_lshlrev_b32_e32 v180, 16, v28
	v_and_b32_e32 v181, 0xffff0000, v28
	v_lshlrev_b32_e32 v182, 16, v29
	v_and_b32_e32 v183, 0xffff0000, v29
	v_lshlrev_b32_e32 v184, 16, v30
	v_and_b32_e32 v185, 0xffff0000, v30
	v_lshlrev_b32_e32 v186, 16, v31
	v_and_b32_e32 v187, 0xffff0000, v31
	s_add_i32 s12, s6, 4
	s_movk_i32 s13, 0xff
	s_cmp_lt_u32 s12, 0x8000
	s_cselect_b32 s13, 0x7ff, s13
	s_and_b32 s16, s12, s13
	s_cmp_lg_u32 s16, 0
	s_cbranch_scc0 .Lp4_nm1_4
	v_pk_fma_f32 v[228:229], v[156:157], v[188:189], v[220:221]
	v_pk_fma_f32 v[230:231], v[158:159], v[190:191], v[222:223]
	v_pk_fma_f32 v[232:233], v[160:161], v[192:193], v[224:225]
	v_pk_fma_f32 v[234:235], v[162:163], v[194:195], v[226:227]
	v_pk_fma_f32 v[228:229], v[164:165], v[196:197], v[228:229]
	v_pk_fma_f32 v[230:231], v[166:167], v[198:199], v[230:231]
	v_pk_fma_f32 v[232:233], v[168:169], v[200:201], v[232:233]
	v_pk_fma_f32 v[234:235], v[170:171], v[202:203], v[234:235]
	s_branch .Lp4_j0_4

.Lp4_j2_4:
	v_cvt_pk_bf16_f32 v236, v228, v229
	v_cvt_pk_bf16_f32 v237, v230, v231
	v_cvt_pk_bf16_f32 v238, v232, v233
	v_cvt_pk_bf16_f32 v239, v234, v235
	s_lshl_b32 s17, s12, 11
	s_add_u32 s2, s8, s17
	s_addc_u32 s3, s9, 0
	global_store_dwordx4 v241, v[236:239], s[2:3]
	s_waitcnt vmcnt(35)
	v_lshlrev_b32_e32 v156, 16, v32
	v_and_b32_e32 v157, 0xffff0000, v32
	v_lshlrev_b32_e32 v158, 16, v33
	v_and_b32_e32 v159, 0xffff0000, v33
	v_lshlrev_b32_e32 v160, 16, v34
	v_and_b32_e32 v161, 0xffff0000, v34
	v_lshlrev_b32_e32 v162, 16, v35
	v_and_b32_e32 v163, 0xffff0000, v35
	s_add_i32 s12, s6, 5
	s_movk_i32 s13, 0xff
	s_cmp_lt_u32 s12, 0x8000
	s_cselect_b32 s13, 0x7ff, s13
	s_and_b32 s16, s12, s13
	s_cmp_lg_u32 s16, 0
	s_cbranch_scc0 .Lp4_nm1_5
	v_pk_fma_f32 v[228:229], v[164:165], v[188:189], v[220:221]
	v_pk_fma_f32 v[230:231], v[166:167], v[190:191], v[222:223]
	v_pk_fma_f32 v[232:233], v[168:169], v[192:193], v[224:225]
	v_pk_fma_f32 v[234:235], v[170:171], v[194:195], v[226:227]
	v_pk_fma_f32 v[228:229], v[172:173], v[196:197], v[228:229]
	v_pk_fma_f32 v[230:231], v[174:175], v[198:199], v[230:231]
	v_pk_fma_f32 v[232:233], v[176:177], v[200:201], v[232:233]
	v_pk_fma_f32 v[234:235], v[178:179], v[202:203], v[234:235]
	s_branch .Lp4_j0_5

.Lp4_j2_5:
	v_cvt_pk_bf16_f32 v236, v228, v229
	v_cvt_pk_bf16_f32 v237, v230, v231
	v_cvt_pk_bf16_f32 v238, v232, v233
	v_cvt_pk_bf16_f32 v239, v234, v235
	s_lshl_b32 s17, s12, 11
	s_add_u32 s2, s8, s17
	s_addc_u32 s3, s9, 0
	global_store_dwordx4 v241, v[236:239], s[2:3]
	s_waitcnt vmcnt(35)
	v_lshlrev_b32_e32 v164, 16, v36
	v_and_b32_e32 v165, 0xffff0000, v36
	v_lshlrev_b32_e32 v166, 16, v37
	v_and_b32_e32 v167, 0xffff0000, v37
	v_lshlrev_b32_e32 v168, 16, v38
	v_and_b32_e32 v169, 0xffff0000, v38
	v_lshlrev_b32_e32 v170, 16, v39
	v_and_b32_e32 v171, 0xffff0000, v39
	s_add_i32 s12, s6, 6
	s_movk_i32 s13, 0xff
	s_cmp_lt_u32 s12, 0x8000
	s_cselect_b32 s13, 0x7ff, s13
	s_and_b32 s16, s12, s13
	s_cmp_lg_u32 s16, 0
	s_cbranch_scc0 .Lp4_nm1_6
	v_pk_fma_f32 v[228:229], v[172:173], v[188:189], v[220:221]
	v_pk_fma_f32 v[230:231], v[174:175], v[190:191], v[222:223]
	v_pk_fma_f32 v[232:233], v[176:177], v[192:193], v[224:225]
	v_pk_fma_f32 v[234:235], v[178:179], v[194:195], v[226:227]
	v_pk_fma_f32 v[228:229], v[180:181], v[196:197], v[228:229]
	v_pk_fma_f32 v[230:231], v[182:183], v[198:199], v[230:231]
	v_pk_fma_f32 v[232:233], v[184:185], v[200:201], v[232:233]
	v_pk_fma_f32 v[234:235], v[186:187], v[202:203], v[234:235]
	s_branch .Lp4_j0_6

.Lp4_j2_6:
	v_cvt_pk_bf16_f32 v236, v228, v229
	v_cvt_pk_bf16_f32 v237, v230, v231
	v_cvt_pk_bf16_f32 v238, v232, v233
	v_cvt_pk_bf16_f32 v239, v234, v235
	s_lshl_b32 s17, s12, 11
	s_add_u32 s2, s8, s17
	s_addc_u32 s3, s9, 0
	global_store_dwordx4 v241, v[236:239], s[2:3]
	s_waitcnt vmcnt(35)
	v_lshlrev_b32_e32 v172, 16, v40
	v_and_b32_e32 v173, 0xffff0000, v40
	v_lshlrev_b32_e32 v174, 16, v41
	v_and_b32_e32 v175, 0xffff0000, v41
	v_lshlrev_b32_e32 v176, 16, v42
	v_and_b32_e32 v177, 0xffff0000, v42
	v_lshlrev_b32_e32 v178, 16, v43
	v_and_b32_e32 v179, 0xffff0000, v43
	s_add_i32 s12, s6, 7
	s_movk_i32 s13, 0xff
	s_cmp_lt_u32 s12, 0x8000
	s_cselect_b32 s13, 0x7ff, s13
	s_and_b32 s16, s12, s13
	s_cmp_lg_u32 s16, 0
	s_cbranch_scc0 .Lp4_nm1_7
	v_pk_fma_f32 v[228:229], v[180:181], v[188:189], v[220:221]
	v_pk_fma_f32 v[230:231], v[182:183], v[190:191], v[222:223]
	v_pk_fma_f32 v[232:233], v[184:185], v[192:193], v[224:225]
	v_pk_fma_f32 v[234:235], v[186:187], v[194:195], v[226:227]
	v_pk_fma_f32 v[228:229], v[156:157], v[196:197], v[228:229]
	v_pk_fma_f32 v[230:231], v[158:159], v[198:199], v[230:231]
	v_pk_fma_f32 v[232:233], v[160:161], v[200:201], v[232:233]
	v_pk_fma_f32 v[234:235], v[162:163], v[202:203], v[234:235]
	s_branch .Lp4_j0_7

.Lp4_j2_7:
	v_cvt_pk_bf16_f32 v236, v228, v229
	v_cvt_pk_bf16_f32 v237, v230, v231
	v_cvt_pk_bf16_f32 v238, v232, v233
	v_cvt_pk_bf16_f32 v239, v234, v235
	s_lshl_b32 s17, s12, 11
	s_add_u32 s2, s8, s17
	s_addc_u32 s3, s9, 0
	global_store_dwordx4 v241, v[236:239], s[2:3]
	s_waitcnt vmcnt(35)
	v_lshlrev_b32_e32 v180, 16, v44
	v_and_b32_e32 v181, 0xffff0000, v44
	v_lshlrev_b32_e32 v182, 16, v45
	v_and_b32_e32 v183, 0xffff0000, v45
	v_lshlrev_b32_e32 v184, 16, v46
	v_and_b32_e32 v185, 0xffff0000, v46
	v_lshlrev_b32_e32 v186, 16, v47
	v_and_b32_e32 v187, 0xffff0000, v47
	s_add_i32 s12, s6, 8
	s_movk_i32 s13, 0xff
	s_cmp_lt_u32 s12, 0x8000
	s_cselect_b32 s13, 0x7ff, s13
	s_and_b32 s16, s12, s13
	s_cmp_lg_u32 s16, 0
	s_cbranch_scc0 .Lp4_nm1_8
	v_pk_fma_f32 v[228:229], v[156:157], v[188:189], v[220:221]
	v_pk_fma_f32 v[230:231], v[158:159], v[190:191], v[222:223]
	v_pk_fma_f32 v[232:233], v[160:161], v[192:193], v[224:225]
	v_pk_fma_f32 v[234:235], v[162:163], v[194:195], v[226:227]
	v_pk_fma_f32 v[228:229], v[164:165], v[196:197], v[228:229]
	v_pk_fma_f32 v[230:231], v[166:167], v[198:199], v[230:231]
	v_pk_fma_f32 v[232:233], v[168:169], v[200:201], v[232:233]
	v_pk_fma_f32 v[234:235], v[170:171], v[202:203], v[234:235]
	s_branch .Lp4_j0_8

.Lp4_j2_8:
	v_cvt_pk_bf16_f32 v236, v228, v229
	v_cvt_pk_bf16_f32 v237, v230, v231
	v_cvt_pk_bf16_f32 v238, v232, v233
	v_cvt_pk_bf16_f32 v239, v234, v235
	s_lshl_b32 s17, s12, 11
	s_add_u32 s2, s8, s17
	s_addc_u32 s3, s9, 0
	global_store_dwordx4 v241, v[236:239], s[2:3]
	s_waitcnt vmcnt(35)
	v_lshlrev_b32_e32 v156, 16, v48
	v_and_b32_e32 v157, 0xffff0000, v48
	v_lshlrev_b32_e32 v158, 16, v49
	v_and_b32_e32 v159, 0xffff0000, v49
	v_lshlrev_b32_e32 v160, 16, v50
	v_and_b32_e32 v161, 0xffff0000, v50
	v_lshlrev_b32_e32 v162, 16, v51
	v_and_b32_e32 v163, 0xffff0000, v51
	s_add_i32 s12, s6, 9
	s_movk_i32 s13, 0xff
	s_cmp_lt_u32 s12, 0x8000
	s_cselect_b32 s13, 0x7ff, s13
	s_and_b32 s16, s12, s13
	s_cmp_lg_u32 s16, 0
	s_cbranch_scc0 .Lp4_nm1_9
	v_pk_fma_f32 v[228:229], v[164:165], v[188:189], v[220:221]
	v_pk_fma_f32 v[230:231], v[166:167], v[190:191], v[222:223]
	v_pk_fma_f32 v[232:233], v[168:169], v[192:193], v[224:225]
	v_pk_fma_f32 v[234:235], v[170:171], v[194:195], v[226:227]
	v_pk_fma_f32 v[228:229], v[172:173], v[196:197], v[228:229]
	v_pk_fma_f32 v[230:231], v[174:175], v[198:199], v[230:231]
	v_pk_fma_f32 v[232:233], v[176:177], v[200:201], v[232:233]
	v_pk_fma_f32 v[234:235], v[178:179], v[202:203], v[234:235]
	s_branch .Lp4_j0_9

.Lp4_j2_9:
	v_cvt_pk_bf16_f32 v236, v228, v229
	v_cvt_pk_bf16_f32 v237, v230, v231
	v_cvt_pk_bf16_f32 v238, v232, v233
	v_cvt_pk_bf16_f32 v239, v234, v235
	s_lshl_b32 s17, s12, 11
	s_add_u32 s2, s8, s17
	s_addc_u32 s3, s9, 0
	global_store_dwordx4 v241, v[236:239], s[2:3]
	s_waitcnt vmcnt(35)
	v_lshlrev_b32_e32 v164, 16, v52
	v_and_b32_e32 v165, 0xffff0000, v52
	v_lshlrev_b32_e32 v166, 16, v53
	v_and_b32_e32 v167, 0xffff0000, v53
	v_lshlrev_b32_e32 v168, 16, v54
	v_and_b32_e32 v169, 0xffff0000, v54
	v_lshlrev_b32_e32 v170, 16, v55
	v_and_b32_e32 v171, 0xffff0000, v55
	s_add_i32 s12, s6, 10
	s_movk_i32 s13, 0xff
	s_cmp_lt_u32 s12, 0x8000
	s_cselect_b32 s13, 0x7ff, s13
	s_and_b32 s16, s12, s13
	s_cmp_lg_u32 s16, 0
	s_cbranch_scc0 .Lp4_nm1_10
	v_pk_fma_f32 v[228:229], v[172:173], v[188:189], v[220:221]
	v_pk_fma_f32 v[230:231], v[174:175], v[190:191], v[222:223]
	v_pk_fma_f32 v[232:233], v[176:177], v[192:193], v[224:225]
	v_pk_fma_f32 v[234:235], v[178:179], v[194:195], v[226:227]
	v_pk_fma_f32 v[228:229], v[180:181], v[196:197], v[228:229]
	v_pk_fma_f32 v[230:231], v[182:183], v[198:199], v[230:231]
	v_pk_fma_f32 v[232:233], v[184:185], v[200:201], v[232:233]
	v_pk_fma_f32 v[234:235], v[186:187], v[202:203], v[234:235]
	s_branch .Lp4_j0_10

.Lp4_j2_10:
	v_cvt_pk_bf16_f32 v236, v228, v229
	v_cvt_pk_bf16_f32 v237, v230, v231
	v_cvt_pk_bf16_f32 v238, v232, v233
	v_cvt_pk_bf16_f32 v239, v234, v235
	s_lshl_b32 s17, s12, 11
	s_add_u32 s2, s8, s17
	s_addc_u32 s3, s9, 0
	global_store_dwordx4 v241, v[236:239], s[2:3]
	s_waitcnt vmcnt(35)
	v_lshlrev_b32_e32 v172, 16, v56
	v_and_b32_e32 v173, 0xffff0000, v56
	v_lshlrev_b32_e32 v174, 16, v57
	v_and_b32_e32 v175, 0xffff0000, v57
	v_lshlrev_b32_e32 v176, 16, v58
	v_and_b32_e32 v177, 0xffff0000, v58
	v_lshlrev_b32_e32 v178, 16, v59
	v_and_b32_e32 v179, 0xffff0000, v59
	s_add_i32 s12, s6, 11
	s_movk_i32 s13, 0xff
	s_cmp_lt_u32 s12, 0x8000
	s_cselect_b32 s13, 0x7ff, s13
	s_and_b32 s16, s12, s13
	s_cmp_lg_u32 s16, 0
	s_cbranch_scc0 .Lp4_nm1_11
	v_pk_fma_f32 v[228:229], v[180:181], v[188:189], v[220:221]
	v_pk_fma_f32 v[230:231], v[182:183], v[190:191], v[222:223]
	v_pk_fma_f32 v[232:233], v[184:185], v[192:193], v[224:225]
	v_pk_fma_f32 v[234:235], v[186:187], v[194:195], v[226:227]
	v_pk_fma_f32 v[228:229], v[156:157], v[196:197], v[228:229]
	v_pk_fma_f32 v[230:231], v[158:159], v[198:199], v[230:231]
	v_pk_fma_f32 v[232:233], v[160:161], v[200:201], v[232:233]
	v_pk_fma_f32 v[234:235], v[162:163], v[202:203], v[234:235]
	s_branch .Lp4_j0_11

.Lp4_j2_11:
	v_cvt_pk_bf16_f32 v236, v228, v229
	v_cvt_pk_bf16_f32 v237, v230, v231
	v_cvt_pk_bf16_f32 v238, v232, v233
	v_cvt_pk_bf16_f32 v239, v234, v235
	s_lshl_b32 s17, s12, 11
	s_add_u32 s2, s8, s17
	s_addc_u32 s3, s9, 0
	global_store_dwordx4 v241, v[236:239], s[2:3]
	s_waitcnt vmcnt(35)
	v_lshlrev_b32_e32 v180, 16, v60
	v_and_b32_e32 v181, 0xffff0000, v60
	v_lshlrev_b32_e32 v182, 16, v61
	v_and_b32_e32 v183, 0xffff0000, v61
	v_lshlrev_b32_e32 v184, 16, v62
	v_and_b32_e32 v185, 0xffff0000, v62
	v_lshlrev_b32_e32 v186, 16, v63
	v_and_b32_e32 v187, 0xffff0000, v63
	s_add_i32 s12, s6, 12
	s_movk_i32 s13, 0xff
	s_cmp_lt_u32 s12, 0x8000
	s_cselect_b32 s13, 0x7ff, s13
	s_and_b32 s16, s12, s13
	s_cmp_lg_u32 s16, 0
	s_cbranch_scc0 .Lp4_nm1_12
	v_pk_fma_f32 v[228:229], v[156:157], v[188:189], v[220:221]
	v_pk_fma_f32 v[230:231], v[158:159], v[190:191], v[222:223]
	v_pk_fma_f32 v[232:233], v[160:161], v[192:193], v[224:225]
	v_pk_fma_f32 v[234:235], v[162:163], v[194:195], v[226:227]
	v_pk_fma_f32 v[228:229], v[164:165], v[196:197], v[228:229]
	v_pk_fma_f32 v[230:231], v[166:167], v[198:199], v[230:231]
	v_pk_fma_f32 v[232:233], v[168:169], v[200:201], v[232:233]
	v_pk_fma_f32 v[234:235], v[170:171], v[202:203], v[234:235]
	s_branch .Lp4_j0_12

.Lp4_j2_12:
	v_cvt_pk_bf16_f32 v236, v228, v229
	v_cvt_pk_bf16_f32 v237, v230, v231
	v_cvt_pk_bf16_f32 v238, v232, v233
	v_cvt_pk_bf16_f32 v239, v234, v235
	s_lshl_b32 s17, s12, 11
	s_add_u32 s2, s8, s17
	s_addc_u32 s3, s9, 0
	global_store_dwordx4 v241, v[236:239], s[2:3]
	s_waitcnt vmcnt(35)
	v_lshlrev_b32_e32 v156, 16, v64
	v_and_b32_e32 v157, 0xffff0000, v64
	v_lshlrev_b32_e32 v158, 16, v65
	v_and_b32_e32 v159, 0xffff0000, v65
	v_lshlrev_b32_e32 v160, 16, v66
	v_and_b32_e32 v161, 0xffff0000, v66
	v_lshlrev_b32_e32 v162, 16, v67
	v_and_b32_e32 v163, 0xffff0000, v67
	s_add_i32 s12, s6, 13
	s_movk_i32 s13, 0xff
	s_cmp_lt_u32 s12, 0x8000
	s_cselect_b32 s13, 0x7ff, s13
	s_and_b32 s16, s12, s13
	s_cmp_lg_u32 s16, 0
	s_cbranch_scc0 .Lp4_nm1_13
	v_pk_fma_f32 v[228:229], v[164:165], v[188:189], v[220:221]
	v_pk_fma_f32 v[230:231], v[166:167], v[190:191], v[222:223]
	v_pk_fma_f32 v[232:233], v[168:169], v[192:193], v[224:225]
	v_pk_fma_f32 v[234:235], v[170:171], v[194:195], v[226:227]
	v_pk_fma_f32 v[228:229], v[172:173], v[196:197], v[228:229]
	v_pk_fma_f32 v[230:231], v[174:175], v[198:199], v[230:231]
	v_pk_fma_f32 v[232:233], v[176:177], v[200:201], v[232:233]
	v_pk_fma_f32 v[234:235], v[178:179], v[202:203], v[234:235]
	s_branch .Lp4_j0_13

.Lp4_j2_13:
	v_cvt_pk_bf16_f32 v236, v228, v229
	v_cvt_pk_bf16_f32 v237, v230, v231
	v_cvt_pk_bf16_f32 v238, v232, v233
	v_cvt_pk_bf16_f32 v239, v234, v235
	s_lshl_b32 s17, s12, 11
	s_add_u32 s2, s8, s17
	s_addc_u32 s3, s9, 0
	global_store_dwordx4 v241, v[236:239], s[2:3]
	s_waitcnt vmcnt(35)
	v_lshlrev_b32_e32 v164, 16, v68
	v_and_b32_e32 v165, 0xffff0000, v68
	v_lshlrev_b32_e32 v166, 16, v69
	v_and_b32_e32 v167, 0xffff0000, v69
	v_lshlrev_b32_e32 v168, 16, v70
	v_and_b32_e32 v169, 0xffff0000, v70
	v_lshlrev_b32_e32 v170, 16, v71
	v_and_b32_e32 v171, 0xffff0000, v71
	s_add_i32 s12, s6, 14
	s_movk_i32 s13, 0xff
	s_cmp_lt_u32 s12, 0x8000
	s_cselect_b32 s13, 0x7ff, s13
	s_and_b32 s16, s12, s13
	s_cmp_lg_u32 s16, 0
	s_cbranch_scc0 .Lp4_nm1_14
	v_pk_fma_f32 v[228:229], v[172:173], v[188:189], v[220:221]
	v_pk_fma_f32 v[230:231], v[174:175], v[190:191], v[222:223]
	v_pk_fma_f32 v[232:233], v[176:177], v[192:193], v[224:225]
	v_pk_fma_f32 v[234:235], v[178:179], v[194:195], v[226:227]
	v_pk_fma_f32 v[228:229], v[180:181], v[196:197], v[228:229]
	v_pk_fma_f32 v[230:231], v[182:183], v[198:199], v[230:231]
	v_pk_fma_f32 v[232:233], v[184:185], v[200:201], v[232:233]
	v_pk_fma_f32 v[234:235], v[186:187], v[202:203], v[234:235]
	s_branch .Lp4_j0_14

.Lp4_j2_14:
	v_cvt_pk_bf16_f32 v236, v228, v229
	v_cvt_pk_bf16_f32 v237, v230, v231
	v_cvt_pk_bf16_f32 v238, v232, v233
	v_cvt_pk_bf16_f32 v239, v234, v235
	s_lshl_b32 s17, s12, 11
	s_add_u32 s2, s8, s17
	s_addc_u32 s3, s9, 0
	global_store_dwordx4 v241, v[236:239], s[2:3]
	s_waitcnt vmcnt(35)
	v_lshlrev_b32_e32 v172, 16, v72
	v_and_b32_e32 v173, 0xffff0000, v72
	v_lshlrev_b32_e32 v174, 16, v73
	v_and_b32_e32 v175, 0xffff0000, v73
	v_lshlrev_b32_e32 v176, 16, v74
	v_and_b32_e32 v177, 0xffff0000, v74
	v_lshlrev_b32_e32 v178, 16, v75
	v_and_b32_e32 v179, 0xffff0000, v75
	s_add_i32 s12, s6, 15
	s_movk_i32 s13, 0xff
	s_cmp_lt_u32 s12, 0x8000
	s_cselect_b32 s13, 0x7ff, s13
	s_and_b32 s16, s12, s13
	s_cmp_lg_u32 s16, 0
	s_cbranch_scc0 .Lp4_nm1_15
	v_pk_fma_f32 v[228:229], v[180:181], v[188:189], v[220:221]
	v_pk_fma_f32 v[230:231], v[182:183], v[190:191], v[222:223]
	v_pk_fma_f32 v[232:233], v[184:185], v[192:193], v[224:225]
	v_pk_fma_f32 v[234:235], v[186:187], v[194:195], v[226:227]
	v_pk_fma_f32 v[228:229], v[156:157], v[196:197], v[228:229]
	v_pk_fma_f32 v[230:231], v[158:159], v[198:199], v[230:231]
	v_pk_fma_f32 v[232:233], v[160:161], v[200:201], v[232:233]
	v_pk_fma_f32 v[234:235], v[162:163], v[202:203], v[234:235]
	s_branch .Lp4_j0_15

.Lp4_j2_15:
	v_cvt_pk_bf16_f32 v236, v228, v229
	v_cvt_pk_bf16_f32 v237, v230, v231
	v_cvt_pk_bf16_f32 v238, v232, v233
	v_cvt_pk_bf16_f32 v239, v234, v235
	s_lshl_b32 s17, s12, 11
	s_add_u32 s2, s8, s17
	s_addc_u32 s3, s9, 0
	global_store_dwordx4 v241, v[236:239], s[2:3]
	s_waitcnt vmcnt(35)
	v_lshlrev_b32_e32 v180, 16, v76
	v_and_b32_e32 v181, 0xffff0000, v76
	v_lshlrev_b32_e32 v182, 16, v77
	v_and_b32_e32 v183, 0xffff0000, v77
	v_lshlrev_b32_e32 v184, 16, v78
	v_and_b32_e32 v185, 0xffff0000, v78
	v_lshlrev_b32_e32 v186, 16, v79
	v_and_b32_e32 v187, 0xffff0000, v79
	s_add_i32 s12, s6, 16
	s_movk_i32 s13, 0xff
	s_cmp_lt_u32 s12, 0x8000
	s_cselect_b32 s13, 0x7ff, s13
	s_and_b32 s16, s12, s13
	s_cmp_lg_u32 s16, 0
	s_cbranch_scc0 .Lp4_nm1_16
	v_pk_fma_f32 v[228:229], v[156:157], v[188:189], v[220:221]
	v_pk_fma_f32 v[230:231], v[158:159], v[190:191], v[222:223]
	v_pk_fma_f32 v[232:233], v[160:161], v[192:193], v[224:225]
	v_pk_fma_f32 v[234:235], v[162:163], v[194:195], v[226:227]
	v_pk_fma_f32 v[228:229], v[164:165], v[196:197], v[228:229]
	v_pk_fma_f32 v[230:231], v[166:167], v[198:199], v[230:231]
	v_pk_fma_f32 v[232:233], v[168:169], v[200:201], v[232:233]
	v_pk_fma_f32 v[234:235], v[170:171], v[202:203], v[234:235]
	s_branch .Lp4_j0_16

.Lp4_j2_16:
	v_cvt_pk_bf16_f32 v236, v228, v229
	v_cvt_pk_bf16_f32 v237, v230, v231
	v_cvt_pk_bf16_f32 v238, v232, v233
	v_cvt_pk_bf16_f32 v239, v234, v235
	s_lshl_b32 s17, s12, 11
	s_add_u32 s2, s8, s17
	s_addc_u32 s3, s9, 0
	global_store_dwordx4 v241, v[236:239], s[2:3]
	s_waitcnt vmcnt(35)
	v_lshlrev_b32_e32 v156, 16, v80
	v_and_b32_e32 v157, 0xffff0000, v80
	v_lshlrev_b32_e32 v158, 16, v81
	v_and_b32_e32 v159, 0xffff0000, v81
	v_lshlrev_b32_e32 v160, 16, v82
	v_and_b32_e32 v161, 0xffff0000, v82
	v_lshlrev_b32_e32 v162, 16, v83
	v_and_b32_e32 v163, 0xffff0000, v83
	s_add_i32 s12, s6, 17
	s_movk_i32 s13, 0xff
	s_cmp_lt_u32 s12, 0x8000
	s_cselect_b32 s13, 0x7ff, s13
	s_and_b32 s16, s12, s13
	s_cmp_lg_u32 s16, 0
	s_cbranch_scc0 .Lp4_nm1_17
	v_pk_fma_f32 v[228:229], v[164:165], v[188:189], v[220:221]
	v_pk_fma_f32 v[230:231], v[166:167], v[190:191], v[222:223]
	v_pk_fma_f32 v[232:233], v[168:169], v[192:193], v[224:225]
	v_pk_fma_f32 v[234:235], v[170:171], v[194:195], v[226:227]
	v_pk_fma_f32 v[228:229], v[172:173], v[196:197], v[228:229]
	v_pk_fma_f32 v[230:231], v[174:175], v[198:199], v[230:231]
	v_pk_fma_f32 v[232:233], v[176:177], v[200:201], v[232:233]
	v_pk_fma_f32 v[234:235], v[178:179], v[202:203], v[234:235]
	s_branch .Lp4_j0_17

.Lp4_j2_17:
	v_cvt_pk_bf16_f32 v236, v228, v229
	v_cvt_pk_bf16_f32 v237, v230, v231
	v_cvt_pk_bf16_f32 v238, v232, v233
	v_cvt_pk_bf16_f32 v239, v234, v235
	s_lshl_b32 s17, s12, 11
	s_add_u32 s2, s8, s17
	s_addc_u32 s3, s9, 0
	global_store_dwordx4 v241, v[236:239], s[2:3]
	s_waitcnt vmcnt(35)
	v_lshlrev_b32_e32 v164, 16, v84
	v_and_b32_e32 v165, 0xffff0000, v84
	v_lshlrev_b32_e32 v166, 16, v85
	v_and_b32_e32 v167, 0xffff0000, v85
	v_lshlrev_b32_e32 v168, 16, v86
	v_and_b32_e32 v169, 0xffff0000, v86
	v_lshlrev_b32_e32 v170, 16, v87
	v_and_b32_e32 v171, 0xffff0000, v87
	s_add_i32 s12, s6, 18
	s_movk_i32 s13, 0xff
	s_cmp_lt_u32 s12, 0x8000
	s_cselect_b32 s13, 0x7ff, s13
	s_and_b32 s16, s12, s13
	s_cmp_lg_u32 s16, 0
	s_cbranch_scc0 .Lp4_nm1_18
	v_pk_fma_f32 v[228:229], v[172:173], v[188:189], v[220:221]
	v_pk_fma_f32 v[230:231], v[174:175], v[190:191], v[222:223]
	v_pk_fma_f32 v[232:233], v[176:177], v[192:193], v[224:225]
	v_pk_fma_f32 v[234:235], v[178:179], v[194:195], v[226:227]
	v_pk_fma_f32 v[228:229], v[180:181], v[196:197], v[228:229]
	v_pk_fma_f32 v[230:231], v[182:183], v[198:199], v[230:231]
	v_pk_fma_f32 v[232:233], v[184:185], v[200:201], v[232:233]
	v_pk_fma_f32 v[234:235], v[186:187], v[202:203], v[234:235]
	s_branch .Lp4_j0_18

.Lp4_j2_18:
	v_cvt_pk_bf16_f32 v236, v228, v229
	v_cvt_pk_bf16_f32 v237, v230, v231
	v_cvt_pk_bf16_f32 v238, v232, v233
	v_cvt_pk_bf16_f32 v239, v234, v235
	s_lshl_b32 s17, s12, 11
	s_add_u32 s2, s8, s17
	s_addc_u32 s3, s9, 0
	global_store_dwordx4 v241, v[236:239], s[2:3]
	s_waitcnt vmcnt(35)
	v_lshlrev_b32_e32 v172, 16, v88
	v_and_b32_e32 v173, 0xffff0000, v88
	v_lshlrev_b32_e32 v174, 16, v89
	v_and_b32_e32 v175, 0xffff0000, v89
	v_lshlrev_b32_e32 v176, 16, v90
	v_and_b32_e32 v177, 0xffff0000, v90
	v_lshlrev_b32_e32 v178, 16, v91
	v_and_b32_e32 v179, 0xffff0000, v91
	s_add_i32 s12, s6, 19
	s_movk_i32 s13, 0xff
	s_cmp_lt_u32 s12, 0x8000
	s_cselect_b32 s13, 0x7ff, s13
	s_and_b32 s16, s12, s13
	s_cmp_lg_u32 s16, 0
	s_cbranch_scc0 .Lp4_nm1_19
	v_pk_fma_f32 v[228:229], v[180:181], v[188:189], v[220:221]
	v_pk_fma_f32 v[230:231], v[182:183], v[190:191], v[222:223]
	v_pk_fma_f32 v[232:233], v[184:185], v[192:193], v[224:225]
	v_pk_fma_f32 v[234:235], v[186:187], v[194:195], v[226:227]
	v_pk_fma_f32 v[228:229], v[156:157], v[196:197], v[228:229]
	v_pk_fma_f32 v[230:231], v[158:159], v[198:199], v[230:231]
	v_pk_fma_f32 v[232:233], v[160:161], v[200:201], v[232:233]
	v_pk_fma_f32 v[234:235], v[162:163], v[202:203], v[234:235]
	s_branch .Lp4_j0_19

.Lp4_j2_19:
	v_cvt_pk_bf16_f32 v236, v228, v229
	v_cvt_pk_bf16_f32 v237, v230, v231
	v_cvt_pk_bf16_f32 v238, v232, v233
	v_cvt_pk_bf16_f32 v239, v234, v235
	s_lshl_b32 s17, s12, 11
	s_add_u32 s2, s8, s17
	s_addc_u32 s3, s9, 0
	global_store_dwordx4 v241, v[236:239], s[2:3]
	s_waitcnt vmcnt(35)
	v_lshlrev_b32_e32 v180, 16, v92
	v_and_b32_e32 v181, 0xffff0000, v92
	v_lshlrev_b32_e32 v182, 16, v93
	v_and_b32_e32 v183, 0xffff0000, v93
	v_lshlrev_b32_e32 v184, 16, v94
	v_and_b32_e32 v185, 0xffff0000, v94
	v_lshlrev_b32_e32 v186, 16, v95
	v_and_b32_e32 v187, 0xffff0000, v95
	s_add_i32 s12, s6, 20
	s_movk_i32 s13, 0xff
	s_cmp_lt_u32 s12, 0x8000
	s_cselect_b32 s13, 0x7ff, s13
	s_and_b32 s16, s12, s13
	s_cmp_lg_u32 s16, 0
	s_cbranch_scc0 .Lp4_nm1_20
	v_pk_fma_f32 v[228:229], v[156:157], v[188:189], v[220:221]
	v_pk_fma_f32 v[230:231], v[158:159], v[190:191], v[222:223]
	v_pk_fma_f32 v[232:233], v[160:161], v[192:193], v[224:225]
	v_pk_fma_f32 v[234:235], v[162:163], v[194:195], v[226:227]
	v_pk_fma_f32 v[228:229], v[164:165], v[196:197], v[228:229]
	v_pk_fma_f32 v[230:231], v[166:167], v[198:199], v[230:231]
	v_pk_fma_f32 v[232:233], v[168:169], v[200:201], v[232:233]
	v_pk_fma_f32 v[234:235], v[170:171], v[202:203], v[234:235]
	s_branch .Lp4_j0_20

.Lp4_j2_20:
	v_cvt_pk_bf16_f32 v236, v228, v229
	v_cvt_pk_bf16_f32 v237, v230, v231
	v_cvt_pk_bf16_f32 v238, v232, v233
	v_cvt_pk_bf16_f32 v239, v234, v235
	s_lshl_b32 s17, s12, 11
	s_add_u32 s2, s8, s17
	s_addc_u32 s3, s9, 0
	global_store_dwordx4 v241, v[236:239], s[2:3]
	s_waitcnt vmcnt(35)
	v_lshlrev_b32_e32 v156, 16, v96
	v_and_b32_e32 v157, 0xffff0000, v96
	v_lshlrev_b32_e32 v158, 16, v97
	v_and_b32_e32 v159, 0xffff0000, v97
	v_lshlrev_b32_e32 v160, 16, v98
	v_and_b32_e32 v161, 0xffff0000, v98
	v_lshlrev_b32_e32 v162, 16, v99
	v_and_b32_e32 v163, 0xffff0000, v99
	s_add_i32 s12, s6, 21
	s_movk_i32 s13, 0xff
	s_cmp_lt_u32 s12, 0x8000
	s_cselect_b32 s13, 0x7ff, s13
	s_and_b32 s16, s12, s13
	s_cmp_lg_u32 s16, 0
	s_cbranch_scc0 .Lp4_nm1_21
	v_pk_fma_f32 v[228:229], v[164:165], v[188:189], v[220:221]
	v_pk_fma_f32 v[230:231], v[166:167], v[190:191], v[222:223]
	v_pk_fma_f32 v[232:233], v[168:169], v[192:193], v[224:225]
	v_pk_fma_f32 v[234:235], v[170:171], v[194:195], v[226:227]
	v_pk_fma_f32 v[228:229], v[172:173], v[196:197], v[228:229]
	v_pk_fma_f32 v[230:231], v[174:175], v[198:199], v[230:231]
	v_pk_fma_f32 v[232:233], v[176:177], v[200:201], v[232:233]
	v_pk_fma_f32 v[234:235], v[178:179], v[202:203], v[234:235]
	s_branch .Lp4_j0_21

.Lp4_j2_21:
	v_cvt_pk_bf16_f32 v236, v228, v229
	v_cvt_pk_bf16_f32 v237, v230, v231
	v_cvt_pk_bf16_f32 v238, v232, v233
	v_cvt_pk_bf16_f32 v239, v234, v235
	s_lshl_b32 s17, s12, 11
	s_add_u32 s2, s8, s17
	s_addc_u32 s3, s9, 0
	global_store_dwordx4 v241, v[236:239], s[2:3]
	s_waitcnt vmcnt(35)
	v_lshlrev_b32_e32 v164, 16, v100
	v_and_b32_e32 v165, 0xffff0000, v100
	v_lshlrev_b32_e32 v166, 16, v101
	v_and_b32_e32 v167, 0xffff0000, v101
	v_lshlrev_b32_e32 v168, 16, v102
	v_and_b32_e32 v169, 0xffff0000, v102
	v_lshlrev_b32_e32 v170, 16, v103
	v_and_b32_e32 v171, 0xffff0000, v103
	s_add_i32 s12, s6, 22
	s_movk_i32 s13, 0xff
	s_cmp_lt_u32 s12, 0x8000
	s_cselect_b32 s13, 0x7ff, s13
	s_and_b32 s16, s12, s13
	s_cmp_lg_u32 s16, 0
	s_cbranch_scc0 .Lp4_nm1_22
	v_pk_fma_f32 v[228:229], v[172:173], v[188:189], v[220:221]
	v_pk_fma_f32 v[230:231], v[174:175], v[190:191], v[222:223]
	v_pk_fma_f32 v[232:233], v[176:177], v[192:193], v[224:225]
	v_pk_fma_f32 v[234:235], v[178:179], v[194:195], v[226:227]
	v_pk_fma_f32 v[228:229], v[180:181], v[196:197], v[228:229]
	v_pk_fma_f32 v[230:231], v[182:183], v[198:199], v[230:231]
	v_pk_fma_f32 v[232:233], v[184:185], v[200:201], v[232:233]
	v_pk_fma_f32 v[234:235], v[186:187], v[202:203], v[234:235]
	s_branch .Lp4_j0_22

.Lp4_j2_22:
	v_cvt_pk_bf16_f32 v236, v228, v229
	v_cvt_pk_bf16_f32 v237, v230, v231
	v_cvt_pk_bf16_f32 v238, v232, v233
	v_cvt_pk_bf16_f32 v239, v234, v235
	s_lshl_b32 s17, s12, 11
	s_add_u32 s2, s8, s17
	s_addc_u32 s3, s9, 0
	global_store_dwordx4 v241, v[236:239], s[2:3]
	s_waitcnt vmcnt(35)
	v_lshlrev_b32_e32 v172, 16, v104
	v_and_b32_e32 v173, 0xffff0000, v104
	v_lshlrev_b32_e32 v174, 16, v105
	v_and_b32_e32 v175, 0xffff0000, v105
	v_lshlrev_b32_e32 v176, 16, v106
	v_and_b32_e32 v177, 0xffff0000, v106
	v_lshlrev_b32_e32 v178, 16, v107
	v_and_b32_e32 v179, 0xffff0000, v107
	s_add_i32 s12, s6, 23
	s_movk_i32 s13, 0xff
	s_cmp_lt_u32 s12, 0x8000
	s_cselect_b32 s13, 0x7ff, s13
	s_and_b32 s16, s12, s13
	s_cmp_lg_u32 s16, 0
	s_cbranch_scc0 .Lp4_nm1_23
	v_pk_fma_f32 v[228:229], v[180:181], v[188:189], v[220:221]
	v_pk_fma_f32 v[230:231], v[182:183], v[190:191], v[222:223]
	v_pk_fma_f32 v[232:233], v[184:185], v[192:193], v[224:225]
	v_pk_fma_f32 v[234:235], v[186:187], v[194:195], v[226:227]
	v_pk_fma_f32 v[228:229], v[156:157], v[196:197], v[228:229]
	v_pk_fma_f32 v[230:231], v[158:159], v[198:199], v[230:231]
	v_pk_fma_f32 v[232:233], v[160:161], v[200:201], v[232:233]
	v_pk_fma_f32 v[234:235], v[162:163], v[202:203], v[234:235]
	s_branch .Lp4_j0_23

.Lp4_j2_23:
	v_cvt_pk_bf16_f32 v236, v228, v229
	v_cvt_pk_bf16_f32 v237, v230, v231
	v_cvt_pk_bf16_f32 v238, v232, v233
	v_cvt_pk_bf16_f32 v239, v234, v235
	s_lshl_b32 s17, s12, 11
	s_add_u32 s2, s8, s17
	s_addc_u32 s3, s9, 0
	global_store_dwordx4 v241, v[236:239], s[2:3]
	s_waitcnt vmcnt(35)
	v_lshlrev_b32_e32 v180, 16, v108
	v_and_b32_e32 v181, 0xffff0000, v108
	v_lshlrev_b32_e32 v182, 16, v109
	v_and_b32_e32 v183, 0xffff0000, v109
	v_lshlrev_b32_e32 v184, 16, v110
	v_and_b32_e32 v185, 0xffff0000, v110
	v_lshlrev_b32_e32 v186, 16, v111
	v_and_b32_e32 v187, 0xffff0000, v111
	s_add_i32 s12, s6, 24
	s_movk_i32 s13, 0xff
	s_cmp_lt_u32 s12, 0x8000
	s_cselect_b32 s13, 0x7ff, s13
	s_and_b32 s16, s12, s13
	s_cmp_lg_u32 s16, 0
	s_cbranch_scc0 .Lp4_nm1_24
	v_pk_fma_f32 v[228:229], v[156:157], v[188:189], v[220:221]
	v_pk_fma_f32 v[230:231], v[158:159], v[190:191], v[222:223]
	v_pk_fma_f32 v[232:233], v[160:161], v[192:193], v[224:225]
	v_pk_fma_f32 v[234:235], v[162:163], v[194:195], v[226:227]
	v_pk_fma_f32 v[228:229], v[164:165], v[196:197], v[228:229]
	v_pk_fma_f32 v[230:231], v[166:167], v[198:199], v[230:231]
	v_pk_fma_f32 v[232:233], v[168:169], v[200:201], v[232:233]
	v_pk_fma_f32 v[234:235], v[170:171], v[202:203], v[234:235]
	s_branch .Lp4_j0_24

.Lp4_j2_24:
	v_cvt_pk_bf16_f32 v236, v228, v229
	v_cvt_pk_bf16_f32 v237, v230, v231
	v_cvt_pk_bf16_f32 v238, v232, v233
	v_cvt_pk_bf16_f32 v239, v234, v235
	s_lshl_b32 s17, s12, 11
	s_add_u32 s2, s8, s17
	s_addc_u32 s3, s9, 0
	global_store_dwordx4 v241, v[236:239], s[2:3]
	s_waitcnt vmcnt(35)
	v_lshlrev_b32_e32 v156, 16, v112
	v_and_b32_e32 v157, 0xffff0000, v112
	v_lshlrev_b32_e32 v158, 16, v113
	v_and_b32_e32 v159, 0xffff0000, v113
	v_lshlrev_b32_e32 v160, 16, v114
	v_and_b32_e32 v161, 0xffff0000, v114
	v_lshlrev_b32_e32 v162, 16, v115
	v_and_b32_e32 v163, 0xffff0000, v115
	s_add_i32 s12, s6, 25
	s_movk_i32 s13, 0xff
	s_cmp_lt_u32 s12, 0x8000
	s_cselect_b32 s13, 0x7ff, s13
	s_and_b32 s16, s12, s13
	s_cmp_lg_u32 s16, 0
	s_cbranch_scc0 .Lp4_nm1_25
	v_pk_fma_f32 v[228:229], v[164:165], v[188:189], v[220:221]
	v_pk_fma_f32 v[230:231], v[166:167], v[190:191], v[222:223]
	v_pk_fma_f32 v[232:233], v[168:169], v[192:193], v[224:225]
	v_pk_fma_f32 v[234:235], v[170:171], v[194:195], v[226:227]
	v_pk_fma_f32 v[228:229], v[172:173], v[196:197], v[228:229]
	v_pk_fma_f32 v[230:231], v[174:175], v[198:199], v[230:231]
	v_pk_fma_f32 v[232:233], v[176:177], v[200:201], v[232:233]
	v_pk_fma_f32 v[234:235], v[178:179], v[202:203], v[234:235]
	s_branch .Lp4_j0_25

.Lp4_j2_25:
	v_cvt_pk_bf16_f32 v236, v228, v229
	v_cvt_pk_bf16_f32 v237, v230, v231
	v_cvt_pk_bf16_f32 v238, v232, v233
	v_cvt_pk_bf16_f32 v239, v234, v235
	s_lshl_b32 s17, s12, 11
	s_add_u32 s2, s8, s17
	s_addc_u32 s3, s9, 0
	global_store_dwordx4 v241, v[236:239], s[2:3]
	s_waitcnt vmcnt(35)
	v_lshlrev_b32_e32 v164, 16, v116
	v_and_b32_e32 v165, 0xffff0000, v116
	v_lshlrev_b32_e32 v166, 16, v117
	v_and_b32_e32 v167, 0xffff0000, v117
	v_lshlrev_b32_e32 v168, 16, v118
	v_and_b32_e32 v169, 0xffff0000, v118
	v_lshlrev_b32_e32 v170, 16, v119
	v_and_b32_e32 v171, 0xffff0000, v119
	s_add_i32 s12, s6, 26
	s_movk_i32 s13, 0xff
	s_cmp_lt_u32 s12, 0x8000
	s_cselect_b32 s13, 0x7ff, s13
	s_and_b32 s16, s12, s13
	s_cmp_lg_u32 s16, 0
	s_cbranch_scc0 .Lp4_nm1_26
	v_pk_fma_f32 v[228:229], v[172:173], v[188:189], v[220:221]
	v_pk_fma_f32 v[230:231], v[174:175], v[190:191], v[222:223]
	v_pk_fma_f32 v[232:233], v[176:177], v[192:193], v[224:225]
	v_pk_fma_f32 v[234:235], v[178:179], v[194:195], v[226:227]
	v_pk_fma_f32 v[228:229], v[180:181], v[196:197], v[228:229]
	v_pk_fma_f32 v[230:231], v[182:183], v[198:199], v[230:231]
	v_pk_fma_f32 v[232:233], v[184:185], v[200:201], v[232:233]
	v_pk_fma_f32 v[234:235], v[186:187], v[202:203], v[234:235]
	s_branch .Lp4_j0_26

.Lp4_j2_26:
	v_cvt_pk_bf16_f32 v236, v228, v229
	v_cvt_pk_bf16_f32 v237, v230, v231
	v_cvt_pk_bf16_f32 v238, v232, v233
	v_cvt_pk_bf16_f32 v239, v234, v235
	s_lshl_b32 s17, s12, 11
	s_add_u32 s2, s8, s17
	s_addc_u32 s3, s9, 0
	global_store_dwordx4 v241, v[236:239], s[2:3]
	s_waitcnt vmcnt(35)
	v_lshlrev_b32_e32 v172, 16, v120
	v_and_b32_e32 v173, 0xffff0000, v120
	v_lshlrev_b32_e32 v174, 16, v121
	v_and_b32_e32 v175, 0xffff0000, v121
	v_lshlrev_b32_e32 v176, 16, v122
	v_and_b32_e32 v177, 0xffff0000, v122
	v_lshlrev_b32_e32 v178, 16, v123
	v_and_b32_e32 v179, 0xffff0000, v123
	s_add_i32 s12, s6, 27
	s_movk_i32 s13, 0xff
	s_cmp_lt_u32 s12, 0x8000
	s_cselect_b32 s13, 0x7ff, s13
	s_and_b32 s16, s12, s13
	s_cmp_lg_u32 s16, 0
	s_cbranch_scc0 .Lp4_nm1_27
	v_pk_fma_f32 v[228:229], v[180:181], v[188:189], v[220:221]
	v_pk_fma_f32 v[230:231], v[182:183], v[190:191], v[222:223]
	v_pk_fma_f32 v[232:233], v[184:185], v[192:193], v[224:225]
	v_pk_fma_f32 v[234:235], v[186:187], v[194:195], v[226:227]
	v_pk_fma_f32 v[228:229], v[156:157], v[196:197], v[228:229]
	v_pk_fma_f32 v[230:231], v[158:159], v[198:199], v[230:231]
	v_pk_fma_f32 v[232:233], v[160:161], v[200:201], v[232:233]
	v_pk_fma_f32 v[234:235], v[162:163], v[202:203], v[234:235]
	s_branch .Lp4_j0_27

.Lp4_j2_27:
	v_cvt_pk_bf16_f32 v236, v228, v229
	v_cvt_pk_bf16_f32 v237, v230, v231
	v_cvt_pk_bf16_f32 v238, v232, v233
	v_cvt_pk_bf16_f32 v239, v234, v235
	s_lshl_b32 s17, s12, 11
	s_add_u32 s2, s8, s17
	s_addc_u32 s3, s9, 0
	global_store_dwordx4 v241, v[236:239], s[2:3]
	s_waitcnt vmcnt(35)
	v_lshlrev_b32_e32 v180, 16, v124
	v_and_b32_e32 v181, 0xffff0000, v124
	v_lshlrev_b32_e32 v182, 16, v125
	v_and_b32_e32 v183, 0xffff0000, v125
	v_lshlrev_b32_e32 v184, 16, v126
	v_and_b32_e32 v185, 0xffff0000, v126
	v_lshlrev_b32_e32 v186, 16, v127
	v_and_b32_e32 v187, 0xffff0000, v127
	s_add_i32 s12, s6, 28
	s_movk_i32 s13, 0xff
	s_cmp_lt_u32 s12, 0x8000
	s_cselect_b32 s13, 0x7ff, s13
	s_and_b32 s16, s12, s13
	s_cmp_lg_u32 s16, 0
	s_cbranch_scc0 .Lp4_nm1_28
	v_pk_fma_f32 v[228:229], v[156:157], v[188:189], v[220:221]
	v_pk_fma_f32 v[230:231], v[158:159], v[190:191], v[222:223]
	v_pk_fma_f32 v[232:233], v[160:161], v[192:193], v[224:225]
	v_pk_fma_f32 v[234:235], v[162:163], v[194:195], v[226:227]
	v_pk_fma_f32 v[228:229], v[164:165], v[196:197], v[228:229]
	v_pk_fma_f32 v[230:231], v[166:167], v[198:199], v[230:231]
	v_pk_fma_f32 v[232:233], v[168:169], v[200:201], v[232:233]
	v_pk_fma_f32 v[234:235], v[170:171], v[202:203], v[234:235]
	s_branch .Lp4_j0_28

.Lp4_j2_28:
	v_cvt_pk_bf16_f32 v236, v228, v229
	v_cvt_pk_bf16_f32 v237, v230, v231
	v_cvt_pk_bf16_f32 v238, v232, v233
	v_cvt_pk_bf16_f32 v239, v234, v235
	s_lshl_b32 s17, s12, 11
	s_add_u32 s2, s8, s17
	s_addc_u32 s3, s9, 0
	global_store_dwordx4 v241, v[236:239], s[2:3]
	s_waitcnt vmcnt(35)
	v_lshlrev_b32_e32 v156, 16, v128
	v_and_b32_e32 v157, 0xffff0000, v128
	v_lshlrev_b32_e32 v158, 16, v129
	v_and_b32_e32 v159, 0xffff0000, v129
	v_lshlrev_b32_e32 v160, 16, v130
	v_and_b32_e32 v161, 0xffff0000, v130
	v_lshlrev_b32_e32 v162, 16, v131
	v_and_b32_e32 v163, 0xffff0000, v131
	s_add_i32 s12, s6, 29
	s_movk_i32 s13, 0xff
	s_cmp_lt_u32 s12, 0x8000
	s_cselect_b32 s13, 0x7ff, s13
	s_and_b32 s16, s12, s13
	s_cmp_lg_u32 s16, 0
	s_cbranch_scc0 .Lp4_nm1_29
	v_pk_fma_f32 v[228:229], v[164:165], v[188:189], v[220:221]
	v_pk_fma_f32 v[230:231], v[166:167], v[190:191], v[222:223]
	v_pk_fma_f32 v[232:233], v[168:169], v[192:193], v[224:225]
	v_pk_fma_f32 v[234:235], v[170:171], v[194:195], v[226:227]
	v_pk_fma_f32 v[228:229], v[172:173], v[196:197], v[228:229]
	v_pk_fma_f32 v[230:231], v[174:175], v[198:199], v[230:231]
	v_pk_fma_f32 v[232:233], v[176:177], v[200:201], v[232:233]
	v_pk_fma_f32 v[234:235], v[178:179], v[202:203], v[234:235]
	s_branch .Lp4_j0_29

.Lp4_j2_29:
	v_cvt_pk_bf16_f32 v236, v228, v229
	v_cvt_pk_bf16_f32 v237, v230, v231
	v_cvt_pk_bf16_f32 v238, v232, v233
	v_cvt_pk_bf16_f32 v239, v234, v235
	s_lshl_b32 s17, s12, 11
	s_add_u32 s2, s8, s17
	s_addc_u32 s3, s9, 0
	global_store_dwordx4 v241, v[236:239], s[2:3]
	s_waitcnt vmcnt(35)
	v_lshlrev_b32_e32 v164, 16, v132
	v_and_b32_e32 v165, 0xffff0000, v132
	v_lshlrev_b32_e32 v166, 16, v133
	v_and_b32_e32 v167, 0xffff0000, v133
	v_lshlrev_b32_e32 v168, 16, v134
	v_and_b32_e32 v169, 0xffff0000, v134
	v_lshlrev_b32_e32 v170, 16, v135
	v_and_b32_e32 v171, 0xffff0000, v135
	s_add_i32 s12, s6, 30
	s_movk_i32 s13, 0xff
	s_cmp_lt_u32 s12, 0x8000
	s_cselect_b32 s13, 0x7ff, s13
	s_and_b32 s16, s12, s13
	s_cmp_lg_u32 s16, 0
	s_cbranch_scc0 .Lp4_nm1_30
	v_pk_fma_f32 v[228:229], v[172:173], v[188:189], v[220:221]
	v_pk_fma_f32 v[230:231], v[174:175], v[190:191], v[222:223]
	v_pk_fma_f32 v[232:233], v[176:177], v[192:193], v[224:225]
	v_pk_fma_f32 v[234:235], v[178:179], v[194:195], v[226:227]
	v_pk_fma_f32 v[228:229], v[180:181], v[196:197], v[228:229]
	v_pk_fma_f32 v[230:231], v[182:183], v[198:199], v[230:231]
	v_pk_fma_f32 v[232:233], v[184:185], v[200:201], v[232:233]
	v_pk_fma_f32 v[234:235], v[186:187], v[202:203], v[234:235]
	s_branch .Lp4_j0_30

.Lp4_j2_30:
	v_cvt_pk_bf16_f32 v236, v228, v229
	v_cvt_pk_bf16_f32 v237, v230, v231
	v_cvt_pk_bf16_f32 v238, v232, v233
	v_cvt_pk_bf16_f32 v239, v234, v235
	s_lshl_b32 s17, s12, 11
	s_add_u32 s2, s8, s17
	s_addc_u32 s3, s9, 0
	global_store_dwordx4 v241, v[236:239], s[2:3]
	s_waitcnt vmcnt(35)
	v_lshlrev_b32_e32 v172, 16, v136
	v_and_b32_e32 v173, 0xffff0000, v136
	v_lshlrev_b32_e32 v174, 16, v137
	v_and_b32_e32 v175, 0xffff0000, v137
	v_lshlrev_b32_e32 v176, 16, v138
	v_and_b32_e32 v177, 0xffff0000, v138
	v_lshlrev_b32_e32 v178, 16, v139
	v_and_b32_e32 v179, 0xffff0000, v139
	s_add_i32 s12, s6, 31
	s_movk_i32 s13, 0xff
	s_cmp_lt_u32 s12, 0x8000
	s_cselect_b32 s13, 0x7ff, s13
	s_and_b32 s16, s12, s13
	s_cmp_lg_u32 s16, 0
	s_cbranch_scc0 .Lp4_nm1_31
	v_pk_fma_f32 v[228:229], v[180:181], v[188:189], v[220:221]
	v_pk_fma_f32 v[230:231], v[182:183], v[190:191], v[222:223]
	v_pk_fma_f32 v[232:233], v[184:185], v[192:193], v[224:225]
	v_pk_fma_f32 v[234:235], v[186:187], v[194:195], v[226:227]
	v_pk_fma_f32 v[228:229], v[156:157], v[196:197], v[228:229]
	v_pk_fma_f32 v[230:231], v[158:159], v[198:199], v[230:231]
	v_pk_fma_f32 v[232:233], v[160:161], v[200:201], v[232:233]
	v_pk_fma_f32 v[234:235], v[162:163], v[202:203], v[234:235]
	s_branch .Lp4_j0_31

.Lp4_j2_31:
	v_cvt_pk_bf16_f32 v236, v228, v229
	v_cvt_pk_bf16_f32 v237, v230, v231
	v_cvt_pk_bf16_f32 v238, v232, v233
	v_cvt_pk_bf16_f32 v239, v234, v235
	s_lshl_b32 s17, s12, 11
	s_add_u32 s2, s8, s17
	s_addc_u32 s3, s9, 0
	global_store_dwordx4 v241, v[236:239], s[2:3]
	s_waitcnt vmcnt(35)
	v_lshlrev_b32_e32 v180, 16, v140
	v_and_b32_e32 v181, 0xffff0000, v140
	v_lshlrev_b32_e32 v182, 16, v141
	v_and_b32_e32 v183, 0xffff0000, v141
	v_lshlrev_b32_e32 v184, 16, v142
	v_and_b32_e32 v185, 0xffff0000, v142
	v_lshlrev_b32_e32 v186, 16, v143
	v_and_b32_e32 v187, 0xffff0000, v143
	s_add_i32 s12, s6, 32
	s_movk_i32 s13, 0xff
	s_cmp_lt_u32 s12, 0x8000
	s_cselect_b32 s13, 0x7ff, s13
	s_and_b32 s16, s12, s13
	s_cmp_lg_u32 s16, 0
	s_cbranch_scc0 .Lp4_nm1_32
	v_pk_fma_f32 v[228:229], v[156:157], v[188:189], v[220:221]
	v_pk_fma_f32 v[230:231], v[158:159], v[190:191], v[222:223]
	v_pk_fma_f32 v[232:233], v[160:161], v[192:193], v[224:225]
	v_pk_fma_f32 v[234:235], v[162:163], v[194:195], v[226:227]
	v_pk_fma_f32 v[228:229], v[164:165], v[196:197], v[228:229]
	v_pk_fma_f32 v[230:231], v[166:167], v[198:199], v[230:231]
	v_pk_fma_f32 v[232:233], v[168:169], v[200:201], v[232:233]
	v_pk_fma_f32 v[234:235], v[170:171], v[202:203], v[234:235]
	s_branch .Lp4_j0_32

.Lp4_j2_32:
	v_cvt_pk_bf16_f32 v236, v228, v229
	v_cvt_pk_bf16_f32 v237, v230, v231
	v_cvt_pk_bf16_f32 v238, v232, v233
	v_cvt_pk_bf16_f32 v239, v234, v235
	s_lshl_b32 s17, s12, 11
	s_add_u32 s2, s8, s17
	s_addc_u32 s3, s9, 0
	global_store_dwordx4 v241, v[236:239], s[2:3]
	s_waitcnt vmcnt(35)
	v_lshlrev_b32_e32 v156, 16, v144
	v_and_b32_e32 v157, 0xffff0000, v144
	v_lshlrev_b32_e32 v158, 16, v145
	v_and_b32_e32 v159, 0xffff0000, v145
	v_lshlrev_b32_e32 v160, 16, v146
	v_and_b32_e32 v161, 0xffff0000, v146
	v_lshlrev_b32_e32 v162, 16, v147
	v_and_b32_e32 v163, 0xffff0000, v147
	s_add_i32 s12, s6, 33
	s_movk_i32 s13, 0xff
	s_cmp_lt_u32 s12, 0x8000
	s_cselect_b32 s13, 0x7ff, s13
	s_and_b32 s16, s12, s13
	s_cmp_lg_u32 s16, 0
	s_cbranch_scc0 .Lp4_nm1_33
	v_pk_fma_f32 v[228:229], v[164:165], v[188:189], v[220:221]
	v_pk_fma_f32 v[230:231], v[166:167], v[190:191], v[222:223]
	v_pk_fma_f32 v[232:233], v[168:169], v[192:193], v[224:225]
	v_pk_fma_f32 v[234:235], v[170:171], v[194:195], v[226:227]
	v_pk_fma_f32 v[228:229], v[172:173], v[196:197], v[228:229]
	v_pk_fma_f32 v[230:231], v[174:175], v[198:199], v[230:231]
	v_pk_fma_f32 v[232:233], v[176:177], v[200:201], v[232:233]
	v_pk_fma_f32 v[234:235], v[178:179], v[202:203], v[234:235]
	s_branch .Lp4_j0_33

.Lp4_j2_33:
	v_cvt_pk_bf16_f32 v236, v228, v229
	v_cvt_pk_bf16_f32 v237, v230, v231
	v_cvt_pk_bf16_f32 v238, v232, v233
	v_cvt_pk_bf16_f32 v239, v234, v235
	s_lshl_b32 s17, s12, 11
	s_add_u32 s2, s8, s17
	s_addc_u32 s3, s9, 0
	global_store_dwordx4 v241, v[236:239], s[2:3]
	s_waitcnt vmcnt(35)
	v_lshlrev_b32_e32 v164, 16, v148
	v_and_b32_e32 v165, 0xffff0000, v148
	v_lshlrev_b32_e32 v166, 16, v149
	v_and_b32_e32 v167, 0xffff0000, v149
	v_lshlrev_b32_e32 v168, 16, v150
	v_and_b32_e32 v169, 0xffff0000, v150
	v_lshlrev_b32_e32 v170, 16, v151
	v_and_b32_e32 v171, 0xffff0000, v151
	s_add_i32 s12, s6, 34
	s_movk_i32 s13, 0xff
	s_cmp_lt_u32 s12, 0x8000
	s_cselect_b32 s13, 0x7ff, s13
	s_and_b32 s16, s12, s13
	s_cmp_lg_u32 s16, 0
	s_cbranch_scc0 .Lp4_nm1_34
	v_pk_fma_f32 v[228:229], v[172:173], v[188:189], v[220:221]
	v_pk_fma_f32 v[230:231], v[174:175], v[190:191], v[222:223]
	v_pk_fma_f32 v[232:233], v[176:177], v[192:193], v[224:225]
	v_pk_fma_f32 v[234:235], v[178:179], v[194:195], v[226:227]
	v_pk_fma_f32 v[228:229], v[180:181], v[196:197], v[228:229]
	v_pk_fma_f32 v[230:231], v[182:183], v[198:199], v[230:231]
	v_pk_fma_f32 v[232:233], v[184:185], v[200:201], v[232:233]
	v_pk_fma_f32 v[234:235], v[186:187], v[202:203], v[234:235]
	s_branch .Lp4_j0_34

.Lp4_j2_34:
	v_cvt_pk_bf16_f32 v236, v228, v229
	v_cvt_pk_bf16_f32 v237, v230, v231
	v_cvt_pk_bf16_f32 v238, v232, v233
	v_cvt_pk_bf16_f32 v239, v234, v235
	s_lshl_b32 s17, s12, 11
	s_add_u32 s2, s8, s17
	s_addc_u32 s3, s9, 0
	global_store_dwordx4 v241, v[236:239], s[2:3]
	s_waitcnt vmcnt(35)
	v_lshlrev_b32_e32 v172, 16, v152
	v_and_b32_e32 v173, 0xffff0000, v152
	v_lshlrev_b32_e32 v174, 16, v153
	v_and_b32_e32 v175, 0xffff0000, v153
	v_lshlrev_b32_e32 v176, 16, v154
	v_and_b32_e32 v177, 0xffff0000, v154
	v_lshlrev_b32_e32 v178, 16, v155
	v_and_b32_e32 v179, 0xffff0000, v155
	s_add_i32 s12, s6, 35
	s_movk_i32 s13, 0xff
	s_cmp_lt_u32 s12, 0x8000
	s_cselect_b32 s13, 0x7ff, s13
	s_and_b32 s16, s12, s13
	s_cmp_lg_u32 s16, 0
	s_cbranch_scc0 .Lp4_nm1_35
	v_pk_fma_f32 v[228:229], v[180:181], v[188:189], v[220:221]
	v_pk_fma_f32 v[230:231], v[182:183], v[190:191], v[222:223]
	v_pk_fma_f32 v[232:233], v[184:185], v[192:193], v[224:225]
	v_pk_fma_f32 v[234:235], v[186:187], v[194:195], v[226:227]
	v_pk_fma_f32 v[228:229], v[156:157], v[196:197], v[228:229]
	v_pk_fma_f32 v[230:231], v[158:159], v[198:199], v[230:231]
	v_pk_fma_f32 v[232:233], v[160:161], v[200:201], v[232:233]
	v_pk_fma_f32 v[234:235], v[162:163], v[202:203], v[234:235]
	s_branch .Lp4_j0_35

.Lp4_j2_35:
	v_cvt_pk_bf16_f32 v236, v228, v229
	v_cvt_pk_bf16_f32 v237, v230, v231
	v_cvt_pk_bf16_f32 v238, v232, v233
	v_cvt_pk_bf16_f32 v239, v234, v235
	s_lshl_b32 s17, s12, 11
	s_add_u32 s2, s8, s17
	s_addc_u32 s3, s9, 0
	global_store_dwordx4 v241, v[236:239], s[2:3]
	s_branch .LBB0_1155
.Lp4_orig:
	v_add_u32_e32 v0, s52, v0
	s_waitcnt vmcnt(0)
	v_lshl_add_u32 v126, s94, 9, v0
	s_mov_b32 s0, 0x480000
	v_cmp_gt_i32_e32 vcc, s0, v126
	s_and_saveexec_b64 s[12:13], vcc
	s_cbranch_execz .LBB0_1154
	s_waitcnt lgkmcnt(0)
	s_load_dwordx4 s[8:11], s[90:91], 0x48
	v_lshlrev_b32_e32 v0, 3, v0
	v_and_b32_e32 v44, 0x3f8, v0
	v_mov_b32_e32 v73, 0
	v_lshlrev_b32_e32 v72, 2, v44
	s_waitcnt lgkmcnt(0)
	v_lshl_add_u64 v[12:13], s[8:9], 0, v[72:73]
	s_mov_b64 s[2:3], 0x1000
	v_lshl_add_u64 v[8:9], v[12:13], 0, s[2:3]
	s_mov_b64 s[2:3], 0x2000
	s_movk_i32 s1, 0x2000
	v_lshl_add_u64 v[10:11], v[12:13], 0, s[2:3]
	s_mov_b64 s[2:3], 0x3000
	v_add_co_u32_e32 v40, vcc, s1, v12
	global_load_dwordx4 v[24:27], v72, s[8:9] offset:16
	global_load_dwordx4 v[28:31], v72, s[8:9]
	v_addc_co_u32_e32 v41, vcc, 0, v13, vcc
	global_load_dwordx4 v[0:3], v[8:9], off offset:16
	global_load_dwordx4 v[4:7], v[40:41], off offset:-4096
	v_lshl_add_u64 v[8:9], v[12:13], 0, s[2:3]
	s_movk_i32 s1, 0x3000
	global_load_dwordx4 v[32:35], v[10:11], off offset:16
	v_add_co_u32_e32 v42, vcc, s1, v12
	global_load_dwordx4 v[8:11], v[8:9], off offset:16
	s_nop 0
	v_addc_co_u32_e32 v43, vcc, 0, v13, vcc
	global_load_dwordx4 v[12:15], v[42:43], off
	global_load_dwordx4 v[36:39], v[40:41], off
	global_load_dwordx4 v[16:19], v72, s[10:11]
	global_load_dwordx4 v[20:23], v72, s[10:11] offset:16
	s_load_dword s10, s[90:91], 0x100
	v_mov_b32_e32 v41, v73
	v_lshlrev_b32_e32 v40, 1, v44
	s_mov_b64 s[6:7], 0x49800000
	s_mov_b64 s[8:9], 0x70800000
	v_lshl_add_u64 v[40:41], s[26:27], 0, v[40:41]
	s_waitcnt lgkmcnt(0)
	s_lshl_b32 s1, s10, 9
	s_lshl_b32 s2, s10, 11
	v_lshl_add_u64 v[74:75], v[40:41], 0, s[6:7]
	v_lshl_add_u64 v[76:77], v[40:41], 0, s[8:9]
	s_lshl_b32 s3, s10, 10
	s_mul_i32 s16, s10, 0x600
	s_mov_b64 s[14:15], 0
	s_mov_b32 s17, 0x8000
	s_mov_b32 s18, 0x47ffff
	v_mov_b32_e32 v127, 0x9000
	v_mov_b32_e32 v128, 0x8fff
	v_mov_b32_e32 v129, 0xff
	v_mov_b32_e32 v130, 0x7ff
	v_mov_b32_e32 v131, 0x100
	v_mov_b32_e32 v132, 0x800
	s_waitcnt vmcnt(9)
	v_mov_b32_e32 v79, v26
	s_waitcnt vmcnt(8)
	v_mov_b32_e32 v81, v28
	v_mov_b32_e32 v83, v29
	v_mov_b32_e32 v85, v30
	v_mov_b32_e32 v87, v31
	v_mov_b32_e32 v89, v24
	v_mov_b32_e32 v91, v25
	v_mov_b32_e32 v93, v27
	v_mov_b32_e32 v94, v26
	v_mov_b32_e32 v96, v28
	v_mov_b32_e32 v98, v30
	v_mov_b32_e32 v100, v24
	s_waitcnt vmcnt(7)
	v_mov_b32_e32 v78, v2
	s_waitcnt vmcnt(6)
	v_mov_b32_e32 v80, v4
	v_mov_b32_e32 v82, v5
	v_mov_b32_e32 v84, v6
	v_mov_b32_e32 v86, v7
	v_mov_b32_e32 v88, v0
	v_mov_b32_e32 v90, v1
	v_mov_b32_e32 v92, v3
	s_waitcnt vmcnt(4)
	v_mov_b32_e32 v102, v10
	v_mov_b32_e32 v103, v34
	s_waitcnt vmcnt(3)
	v_mov_b32_e32 v104, v12
	s_waitcnt vmcnt(2)
	v_mov_b32_e32 v105, v36
	v_mov_b32_e32 v106, v13
	v_mov_b32_e32 v107, v37
	v_mov_b32_e32 v108, v14
	v_mov_b32_e32 v109, v38
	v_mov_b32_e32 v110, v15
	v_mov_b32_e32 v111, v39
	v_mov_b32_e32 v112, v8
	v_mov_b32_e32 v113, v32
	v_mov_b32_e32 v114, v9
	v_mov_b32_e32 v115, v33
	v_mov_b32_e32 v116, v11
	v_mov_b32_e32 v117, v35
	v_mov_b32_e32 v95, v2
	v_mov_b32_e32 v97, v4
	v_mov_b32_e32 v4, v29
	v_mov_b32_e32 v99, v6
	v_mov_b32_e32 v6, v31
	v_mov_b32_e32 v101, v0
	v_mov_b32_e32 v0, v25
	v_mov_b32_e32 v2, v27
	v_mov_b32_e32 v118, v34
	v_mov_b32_e32 v119, v10
	v_mov_b32_e32 v120, v36
	v_mov_b32_e32 v121, v12
	v_mov_b32_e32 v12, v37
	v_mov_b32_e32 v122, v38
	v_mov_b32_e32 v123, v14
	v_mov_b32_e32 v14, v39
	v_mov_b32_e32 v124, v32
	v_mov_b32_e32 v125, v8
	v_mov_b32_e32 v8, v33
	v_mov_b32_e32 v10, v35
	s_branch .LBB0_1148
